# out-proj epilogue: residual loads hoisted 16-deep with loads-only counted waits (hazard padding kept); S5 epilogue waits made loads-only
# baseline (speedup 1.0000x reference)
; __device__ __forceinline__ unsigned pk2(float lo, float hi) { const f32x2 v = {lo, hi}; return __builtin_bit_cast(unsigned, __builtin_convertvector(v, bf16x2_t)); }
;     __device__ __forceinline__ void operator()(const f32x4 (&acc)[2][2][4][2], const pg::Unit& u, int wr, int wc, int fr, int fq) const {
;         const int colb = u.pn * 256 + wc * 32 + 8 * fq;
;         f32x4 gv[2][2];
; #pragma unroll
;         for (int bj = 0; bj < 2; ++bj)
; #pragma unroll
;             for (int n = 0; n < 2; ++n) gv[bj][n] = *(const f32x4*)(g + colb + bj * 128 + n * 4);
; #pragma unroll
;         for (int ai = 0; ai < 2; ++ai)
; #pragma unroll
;             for (int m = 0; m < 4; ++m) { const int row = u.pm * 256 + ai * 128 + wr * 64 + m * 16 + fr; const size_t off = (size_t)row * D_ + colb;
; #pragma unroll
;                 for (int bj = 0; bj < 2; ++bj) { f32x4 o[2];
; #pragma unroll
;                     for (int n = 0; n < 2; ++n) { const f32x4 r = *(const f32x4*)(R + off + bj * 128 + n * 4); o[n] = r + acc[ai][bj][m][n]; *(f32x4*)(O + off + bj * 128 + n * 4) = o[n]; }
;                     u32x4 w; w.x = pk2(o[0][0] * gv[bj][0][0], o[0][1] * gv[bj][0][1]); w.y = pk2(o[0][2] * gv[bj][0][2], o[0][3] * gv[bj][0][3]);
;                     w.z = pk2(o[1][0] * gv[bj][1][0], o[1][1] * gv[bj][1][1]); w.w = pk2(o[1][2] * gv[bj][1][2], o[1][3] * gv[bj][1][3]);
;                     *(u32x4*)(HBo + off + bj * 128) = w; } }
.LBB0_657:
	v_lshl_add_u32 v152, s36, 8, v154
	v_lshl_add_u32 v150, s37, 8, v156
	v_ashrrev_i32_e32 v153, 31, v152
	v_ashrrev_i32_e32 v151, 31, v150
	v_lshlrev_b64 v[116:117], 11, v[152:153]
	v_readlane_b32 s48, v254, 11
	v_lshl_add_u64 v[164:165], v[116:117], 0, v[150:151]
	v_readlane_b32 s49, v254, 12
	v_lshlrev_b64 v[166:167], 2, v[164:165]
	v_readlane_b32 s50, v254, 13
	v_readlane_b32 s51, v254, 14
	v_readlane_b32 s52, v254, 15
	v_readlane_b32 s53, v254, 16
	v_readlane_b32 s54, v254, 17
	v_readlane_b32 s55, v254, 18
	v_readlane_b32 s56, v254, 19
	v_readlane_b32 s57, v254, 20
	s_mov_b64 s[36:37], s[48:49]
	v_lshl_add_u64 v[168:169], s[36:37], 0, v[166:167]
	s_nop 0
	s_mov_b64 s[40:41], s[52:53]
	v_lshl_add_u64 v[120:121], v[150:151], 2, s[40:41]
	v_lshl_add_u64 v[166:167], s[10:11], 0, v[166:167]
	global_load_dwordx4 v[128:131], v[120:121], off offset:16
	global_load_dwordx4 v[132:135], v[120:121], off
	global_load_dwordx4 v[116:119], v[120:121], off offset:528
	s_nop 0
	global_load_dwordx4 v[120:123], v[120:121], off offset:512
	v_mov_b32_e32 v170, v168
	v_mov_b32_e32 v171, v169
	v_add_co_u32_e32 v172, vcc, 0x20000, v168
	s_nop 1
	v_addc_co_u32_e32 v173, vcc, 0, v169, vcc
	v_add_co_u32_e32 v174, vcc, 0x40000, v168
	s_nop 1
	v_addc_co_u32_e32 v175, vcc, 0, v169, vcc
	v_add_co_u32_e32 v176, vcc, 0x60000, v168
	s_nop 1
	v_addc_co_u32_e32 v177, vcc, 0, v169, vcc
	v_add_co_u32_e32 v178, vcc, 0x100000, v168
	s_nop 1
	v_addc_co_u32_e32 v179, vcc, 0, v169, vcc
	v_add_co_u32_e32 v180, vcc, 0x120000, v168
	s_nop 1
	v_addc_co_u32_e32 v181, vcc, 0, v169, vcc
	v_add_co_u32_e32 v182, vcc, 0x140000, v168
	s_nop 1
	v_addc_co_u32_e32 v183, vcc, 0, v169, vcc
	v_add_co_u32_e32 v184, vcc, 0x160000, v168
	s_nop 1
	v_addc_co_u32_e32 v185, vcc, 0, v169, vcc
	global_load_dwordx4 v[186:189], v[170:171], off
	global_load_dwordx4 v[190:193], v[170:171], off offset:16
	global_load_dwordx4 v[194:197], v[170:171], off offset:512
	global_load_dwordx4 v[198:201], v[170:171], off offset:528
	global_load_dwordx4 v[202:205], v[172:173], off
	global_load_dwordx4 v[206:209], v[172:173], off offset:16
	global_load_dwordx4 v[210:213], v[172:173], off offset:512
	global_load_dwordx4 v[214:217], v[172:173], off offset:528
	global_load_dwordx4 v[218:221], v[174:175], off
	global_load_dwordx4 v[222:225], v[174:175], off offset:16
	global_load_dwordx4 v[226:229], v[174:175], off offset:512
	global_load_dwordx4 v[230:233], v[174:175], off offset:528
	global_load_dwordx4 v[234:237], v[176:177], off
	global_load_dwordx4 v[238:241], v[176:177], off offset:16
	global_load_dwordx4 v[242:245], v[176:177], off offset:512
	global_load_dwordx4 v[246:249], v[176:177], off offset:528
	v_lshl_add_u64 v[164:165], v[164:165], 1, s[12:13]
	s_andn2_b64 vcc, exec, s[16:17]
	s_mov_b64 s[16:17], -1
	v_readlane_b32 s58, v254, 21
	v_readlane_b32 s59, v254, 22
	v_readlane_b32 s60, v254, 23
	v_readlane_b32 s61, v254, 24
	v_readlane_b32 s62, v254, 25
	v_readlane_b32 s63, v254, 26
	s_mov_b64 s[38:39], s[50:51]
	s_mov_b64 s[42:43], s[54:55]
	s_mov_b64 s[44:45], s[56:57]
	s_waitcnt vmcnt(15)
	v_mov_b32_e32 v160, v186
	v_mov_b32_e32 v161, v187
	v_mov_b32_e32 v162, v188
	v_mov_b32_e32 v163, v189
	v_pk_add_f32 v[142:143], v[142:143], v[162:163]
	v_pk_add_f32 v[140:141], v[140:141], v[160:161]
	global_store_dwordx4 v[166:167], v[140:143], off
	s_nop 0
	s_waitcnt vmcnt(14)
	v_mov_b32_e32 v160, v190
	v_mov_b32_e32 v161, v191
	v_mov_b32_e32 v162, v192
	v_mov_b32_e32 v163, v193
	v_pk_add_f32 v[138:139], v[138:139], v[162:163]
	v_pk_add_f32 v[136:137], v[136:137], v[160:161]
	v_pk_mul_f32 v[142:143], v[134:135], v[142:143]
	v_pk_mul_f32 v[140:141], v[132:133], v[140:141]
	global_store_dwordx4 v[166:167], v[136:139], off offset:16
	v_cvt_pk_bf16_f32 v140, v140, v141
	v_cvt_pk_bf16_f32 v141, v142, v143
	v_pk_mul_f32 v[138:139], v[130:131], v[138:139]
	v_pk_mul_f32 v[136:137], v[128:129], v[136:137]
	v_cvt_pk_bf16_f32 v143, v138, v139
	v_cvt_pk_bf16_f32 v142, v136, v137
	global_store_dwordx4 v[164:165], v[140:143], off
	s_nop 0
	s_waitcnt vmcnt(13)
	v_mov_b32_e32 v136, v194
	v_mov_b32_e32 v137, v195
	v_mov_b32_e32 v138, v196
	v_mov_b32_e32 v139, v197
	v_pk_add_f32 v[126:127], v[126:127], v[138:139]
	v_pk_add_f32 v[124:125], v[124:125], v[136:137]
	global_store_dwordx4 v[166:167], v[124:127], off offset:512
	s_nop 0
	v_or_b32_e32 v140, 16, v152
	v_ashrrev_i32_e32 v141, 31, v140
	v_lshlrev_b64 v[140:141], 11, v[140:141]
	v_lshl_add_u64 v[140:141], v[140:141], 0, v[150:151]
	v_pk_mul_f32 v[126:127], v[122:123], v[126:127]
	v_pk_mul_f32 v[124:125], v[120:121], v[124:125]
	v_lshlrev_b64 v[142:143], 2, v[140:141]
	v_cvt_pk_bf16_f32 v124, v124, v125
	v_cvt_pk_bf16_f32 v125, v126, v127
	v_lshl_add_u64 v[160:161], s[36:37], 0, v[142:143]
	s_waitcnt vmcnt(12)
	v_mov_b32_e32 v136, v198
	v_mov_b32_e32 v137, v199
	v_mov_b32_e32 v138, v200
	v_mov_b32_e32 v139, v201
	global_load_dwordx4 v[186:189], v[178:179], off
	global_load_dwordx4 v[190:193], v[178:179], off offset:16
	global_load_dwordx4 v[194:197], v[178:179], off offset:512
	global_load_dwordx4 v[198:201], v[178:179], off offset:528
	v_pk_add_f32 v[110:111], v[110:111], v[138:139]
	v_pk_add_f32 v[108:109], v[108:109], v[136:137]
	global_store_dwordx4 v[166:167], v[108:111], off offset:528
	s_nop 1
	v_pk_mul_f32 v[110:111], v[118:119], v[110:111]
	v_pk_mul_f32 v[108:109], v[116:117], v[108:109]
	v_cvt_pk_bf16_f32 v127, v110, v111
	v_cvt_pk_bf16_f32 v126, v108, v109
	global_store_dwordx4 v[164:165], v[124:127], off offset:256
	s_nop 0
	s_waitcnt vmcnt(15)
; __device__ __forceinline__ unsigned pk2(float lo, float hi) { const f32x2 v = {lo, hi}; return __builtin_bit_cast(unsigned, __builtin_convertvector(v, bf16x2_t)); }
;     __device__ __forceinline__ void operator()(const f32x4 (&acc)[2][2][4][2], const pg::Unit& u, int wr, int wc, int fr, int fq) const {
;         const int colb = u.pn * 256 + wc * 32 + 8 * fq;
;         f32x4 gv[2][2];
; #pragma unroll
;         for (int bj = 0; bj < 2; ++bj)
; #pragma unroll
;             for (int n = 0; n < 2; ++n) gv[bj][n] = *(const f32x4*)(g + colb + bj * 128 + n * 4);
; #pragma unroll
;         for (int ai = 0; ai < 2; ++ai)
; #pragma unroll
;             for (int m = 0; m < 4; ++m) { const int row = u.pm * 256 + ai * 128 + wr * 64 + m * 16 + fr; const size_t off = (size_t)row * D_ + colb;
; #pragma unroll
;                 for (int bj = 0; bj < 2; ++bj) { f32x4 o[2];
; #pragma unroll
;                     for (int n = 0; n < 2; ++n) { const f32x4 r = *(const f32x4*)(R + off + bj * 128 + n * 4); o[n] = r + acc[ai][bj][m][n]; *(f32x4*)(O + off + bj * 128 + n * 4) = o[n]; }
;                     u32x4 w; w.x = pk2(o[0][0] * gv[bj][0][0], o[0][1] * gv[bj][0][1]); w.y = pk2(o[0][2] * gv[bj][0][2], o[0][3] * gv[bj][0][3]);
;                     w.z = pk2(o[1][0] * gv[bj][1][0], o[1][1] * gv[bj][1][1]); w.w = pk2(o[1][2] * gv[bj][1][2], o[1][3] * gv[bj][1][3]);
;                     *(u32x4*)(HBo + off + bj * 128) = w; } }
	v_mov_b32_e32 v108, v202
	v_mov_b32_e32 v109, v203
	v_mov_b32_e32 v110, v204
	v_mov_b32_e32 v111, v205
	v_pk_add_f32 v[110:111], v[114:115], v[110:111]
	v_lshl_add_u64 v[124:125], s[10:11], 0, v[142:143]
	v_pk_add_f32 v[108:109], v[112:113], v[108:109]
	global_store_dwordx4 v[124:125], v[108:111], off
	s_nop 0
	v_lshl_add_u64 v[126:127], v[140:141], 1, s[12:13]
	v_pk_mul_f32 v[110:111], v[134:135], v[110:111]
	v_pk_mul_f32 v[108:109], v[132:133], v[108:109]
	s_waitcnt vmcnt(14)
	v_mov_b32_e32 v112, v206
	v_mov_b32_e32 v113, v207
	v_mov_b32_e32 v114, v208
	v_mov_b32_e32 v115, v209
	v_pk_add_f32 v[106:107], v[106:107], v[114:115]
	v_pk_add_f32 v[104:105], v[104:105], v[112:113]
	global_store_dwordx4 v[124:125], v[104:107], off offset:16
	v_cvt_pk_bf16_f32 v108, v108, v109
	v_cvt_pk_bf16_f32 v109, v110, v111
	v_pk_mul_f32 v[106:107], v[130:131], v[106:107]
	v_pk_mul_f32 v[104:105], v[128:129], v[104:105]
	v_cvt_pk_bf16_f32 v111, v106, v107
	v_cvt_pk_bf16_f32 v110, v104, v105
	global_store_dwordx4 v[126:127], v[108:111], off
	s_nop 0
	s_waitcnt vmcnt(13)
	v_mov_b32_e32 v104, v210
	v_mov_b32_e32 v105, v211
	v_mov_b32_e32 v106, v212
	v_mov_b32_e32 v107, v213
	v_pk_add_f32 v[102:103], v[102:103], v[106:107]
	v_pk_add_f32 v[100:101], v[100:101], v[104:105]
	global_store_dwordx4 v[124:125], v[100:103], off offset:512
	s_nop 0
	v_or_b32_e32 v108, 32, v152
	v_ashrrev_i32_e32 v109, 31, v108
	v_lshlrev_b64 v[108:109], 11, v[108:109]
	v_lshl_add_u64 v[108:109], v[108:109], 0, v[150:151]
	v_pk_mul_f32 v[102:103], v[122:123], v[102:103]
	v_pk_mul_f32 v[100:101], v[120:121], v[100:101]
	v_lshlrev_b64 v[110:111], 2, v[108:109]
	v_cvt_pk_bf16_f32 v100, v100, v101
	v_cvt_pk_bf16_f32 v101, v102, v103
	v_lshl_add_u64 v[112:113], s[36:37], 0, v[110:111]
	s_waitcnt vmcnt(12)
	v_mov_b32_e32 v104, v214
	v_mov_b32_e32 v105, v215
	v_mov_b32_e32 v106, v216
	v_mov_b32_e32 v107, v217
	global_load_dwordx4 v[202:205], v[180:181], off
	global_load_dwordx4 v[206:209], v[180:181], off offset:16
	global_load_dwordx4 v[210:213], v[180:181], off offset:512
	global_load_dwordx4 v[214:217], v[180:181], off offset:528
	v_pk_add_f32 v[94:95], v[94:95], v[106:107]
	v_pk_add_f32 v[92:93], v[92:93], v[104:105]
	global_store_dwordx4 v[124:125], v[92:95], off offset:528
	s_nop 1
	v_pk_mul_f32 v[94:95], v[118:119], v[94:95]
	v_pk_mul_f32 v[92:93], v[116:117], v[92:93]
	v_cvt_pk_bf16_f32 v103, v94, v95
	v_cvt_pk_bf16_f32 v102, v92, v93
	global_store_dwordx4 v[126:127], v[100:103], off offset:256
	s_nop 0
	s_waitcnt vmcnt(15)
	v_mov_b32_e32 v92, v218
	v_mov_b32_e32 v93, v219
	v_mov_b32_e32 v94, v220
	v_mov_b32_e32 v95, v221
	v_pk_add_f32 v[94:95], v[98:99], v[94:95]
	v_lshl_add_u64 v[100:101], s[10:11], 0, v[110:111]
	v_pk_add_f32 v[92:93], v[96:97], v[92:93]
	global_store_dwordx4 v[100:101], v[92:95], off
	s_nop 0
	v_lshl_add_u64 v[102:103], v[108:109], 1, s[12:13]
	v_pk_mul_f32 v[94:95], v[134:135], v[94:95]
	v_pk_mul_f32 v[92:93], v[132:133], v[92:93]
	s_waitcnt vmcnt(14)
	v_mov_b32_e32 v96, v222
	v_mov_b32_e32 v97, v223
	v_mov_b32_e32 v98, v224
	v_mov_b32_e32 v99, v225
	v_pk_add_f32 v[90:91], v[90:91], v[98:99]
	v_pk_add_f32 v[88:89], v[88:89], v[96:97]
	global_store_dwordx4 v[100:101], v[88:91], off offset:16
	v_cvt_pk_bf16_f32 v92, v92, v93
	v_cvt_pk_bf16_f32 v93, v94, v95
	v_pk_mul_f32 v[90:91], v[130:131], v[90:91]
	v_pk_mul_f32 v[88:89], v[128:129], v[88:89]
	v_cvt_pk_bf16_f32 v95, v90, v91
	v_cvt_pk_bf16_f32 v94, v88, v89
	global_store_dwordx4 v[102:103], v[92:95], off
	s_nop 0
	s_waitcnt vmcnt(13)
	v_mov_b32_e32 v88, v226
	v_mov_b32_e32 v89, v227
	v_mov_b32_e32 v90, v228
	v_mov_b32_e32 v91, v229
	v_pk_add_f32 v[86:87], v[86:87], v[90:91]
	v_pk_add_f32 v[84:85], v[84:85], v[88:89]
	global_store_dwordx4 v[100:101], v[84:87], off offset:512
	s_nop 0
	v_or_b32_e32 v92, 48, v152
	v_ashrrev_i32_e32 v93, 31, v92
	v_lshlrev_b64 v[92:93], 11, v[92:93]
	v_lshl_add_u64 v[92:93], v[92:93], 0, v[150:151]
	v_pk_mul_f32 v[86:87], v[122:123], v[86:87]
	v_pk_mul_f32 v[84:85], v[120:121], v[84:85]
	v_lshlrev_b64 v[94:95], 2, v[92:93]
	v_cvt_pk_bf16_f32 v84, v84, v85
	v_cvt_pk_bf16_f32 v85, v86, v87
	v_lshl_add_u64 v[96:97], s[36:37], 0, v[94:95]
	s_waitcnt vmcnt(12)
	v_mov_b32_e32 v88, v230
	v_mov_b32_e32 v89, v231
	v_mov_b32_e32 v90, v232
	v_mov_b32_e32 v91, v233
	global_load_dwordx4 v[218:221], v[182:183], off
	global_load_dwordx4 v[222:225], v[182:183], off offset:16
	global_load_dwordx4 v[226:229], v[182:183], off offset:512
	global_load_dwordx4 v[230:233], v[182:183], off offset:528
	v_pk_add_f32 v[78:79], v[78:79], v[90:91]
	v_pk_add_f32 v[76:77], v[76:77], v[88:89]
	global_store_dwordx4 v[100:101], v[76:79], off offset:528
	s_nop 1
	v_pk_mul_f32 v[78:79], v[118:119], v[78:79]
	v_pk_mul_f32 v[76:77], v[116:117], v[76:77]
	v_cvt_pk_bf16_f32 v87, v78, v79
	v_cvt_pk_bf16_f32 v86, v76, v77
	global_store_dwordx4 v[102:103], v[84:87], off offset:256
	s_nop 0
	s_waitcnt vmcnt(15)
	v_mov_b32_e32 v76, v234
	v_mov_b32_e32 v77, v235
	v_mov_b32_e32 v78, v236
	v_mov_b32_e32 v79, v237
	v_pk_add_f32 v[78:79], v[82:83], v[78:79]
	v_lshl_add_u64 v[84:85], s[10:11], 0, v[94:95]
	v_pk_add_f32 v[76:77], v[80:81], v[76:77]
	global_store_dwordx4 v[84:85], v[76:79], off
	s_nop 0
	v_lshl_add_u64 v[86:87], v[92:93], 1, s[12:13]
	v_pk_mul_f32 v[78:79], v[134:135], v[78:79]
	v_pk_mul_f32 v[76:77], v[132:133], v[76:77]
	s_waitcnt vmcnt(14)
	v_mov_b32_e32 v80, v238
	v_mov_b32_e32 v81, v239
	v_mov_b32_e32 v82, v240
	v_mov_b32_e32 v83, v241
	v_pk_add_f32 v[74:75], v[74:75], v[82:83]
	v_pk_add_f32 v[72:73], v[72:73], v[80:81]
	global_store_dwordx4 v[84:85], v[72:75], off offset:16
	v_cvt_pk_bf16_f32 v76, v76, v77
	v_cvt_pk_bf16_f32 v77, v78, v79
	v_pk_mul_f32 v[74:75], v[130:131], v[74:75]
	v_pk_mul_f32 v[72:73], v[128:129], v[72:73]
	v_cvt_pk_bf16_f32 v79, v74, v75
	v_cvt_pk_bf16_f32 v78, v72, v73
	global_store_dwordx4 v[86:87], v[76:79], off
	s_nop 0
	s_waitcnt vmcnt(13)
; __device__ __forceinline__ unsigned pk2(float lo, float hi) { const f32x2 v = {lo, hi}; return __builtin_bit_cast(unsigned, __builtin_convertvector(v, bf16x2_t)); }
;     __device__ __forceinline__ void operator()(const f32x4 (&acc)[2][2][4][2], const pg::Unit& u, int wr, int wc, int fr, int fq) const {
;         const int colb = u.pn * 256 + wc * 32 + 8 * fq;
;         f32x4 gv[2][2];
; #pragma unroll
;         for (int bj = 0; bj < 2; ++bj)
; #pragma unroll
;             for (int n = 0; n < 2; ++n) gv[bj][n] = *(const f32x4*)(g + colb + bj * 128 + n * 4);
; #pragma unroll
;         for (int ai = 0; ai < 2; ++ai)
; #pragma unroll
;             for (int m = 0; m < 4; ++m) { const int row = u.pm * 256 + ai * 128 + wr * 64 + m * 16 + fr; const size_t off = (size_t)row * D_ + colb;
; #pragma unroll
;                 for (int bj = 0; bj < 2; ++bj) { f32x4 o[2];
; #pragma unroll
;                     for (int n = 0; n < 2; ++n) { const f32x4 r = *(const f32x4*)(R + off + bj * 128 + n * 4); o[n] = r + acc[ai][bj][m][n]; *(f32x4*)(O + off + bj * 128 + n * 4) = o[n]; }
;                     u32x4 w; w.x = pk2(o[0][0] * gv[bj][0][0], o[0][1] * gv[bj][0][1]); w.y = pk2(o[0][2] * gv[bj][0][2], o[0][3] * gv[bj][0][3]);
;                     w.z = pk2(o[1][0] * gv[bj][1][0], o[1][1] * gv[bj][1][1]); w.w = pk2(o[1][2] * gv[bj][1][2], o[1][3] * gv[bj][1][3]);
;                     *(u32x4*)(HBo + off + bj * 128) = w; } }
	v_mov_b32_e32 v72, v242
	v_mov_b32_e32 v73, v243
	v_mov_b32_e32 v74, v244
	v_mov_b32_e32 v75, v245
	v_pk_add_f32 v[70:71], v[70:71], v[74:75]
	v_pk_add_f32 v[68:69], v[68:69], v[72:73]
	global_store_dwordx4 v[84:85], v[68:71], off offset:512
	s_nop 0
	v_add_u32_e32 v76, 0x80, v152
	v_ashrrev_i32_e32 v77, 31, v76
	v_lshlrev_b64 v[76:77], 11, v[76:77]
	v_lshl_add_u64 v[76:77], v[76:77], 0, v[150:151]
	v_pk_mul_f32 v[70:71], v[122:123], v[70:71]
	v_pk_mul_f32 v[68:69], v[120:121], v[68:69]
	v_lshlrev_b64 v[78:79], 2, v[76:77]
	v_cvt_pk_bf16_f32 v68, v68, v69
	v_cvt_pk_bf16_f32 v69, v70, v71
	v_lshl_add_u64 v[80:81], s[36:37], 0, v[78:79]
	s_waitcnt vmcnt(12)
	v_mov_b32_e32 v72, v246
	v_mov_b32_e32 v73, v247
	v_mov_b32_e32 v74, v248
	v_mov_b32_e32 v75, v249
	global_load_dwordx4 v[234:237], v[184:185], off
	global_load_dwordx4 v[238:241], v[184:185], off offset:16
	global_load_dwordx4 v[242:245], v[184:185], off offset:512
	global_load_dwordx4 v[246:249], v[184:185], off offset:528
	v_pk_add_f32 v[66:67], v[66:67], v[74:75]
	v_pk_add_f32 v[64:65], v[64:65], v[72:73]
	global_store_dwordx4 v[84:85], v[64:67], off offset:528
	s_nop 1
	v_pk_mul_f32 v[66:67], v[118:119], v[66:67]
	v_pk_mul_f32 v[64:65], v[116:117], v[64:65]
	v_cvt_pk_bf16_f32 v71, v66, v67
	v_cvt_pk_bf16_f32 v70, v64, v65
	global_store_dwordx4 v[86:87], v[68:71], off offset:256
	s_nop 0
	s_waitcnt vmcnt(15)
	v_mov_b32_e32 v64, v186
	v_mov_b32_e32 v65, v187
	v_mov_b32_e32 v66, v188
	v_mov_b32_e32 v67, v189
	v_pk_add_f32 v[62:63], v[62:63], v[66:67]
	v_lshl_add_u64 v[68:69], s[10:11], 0, v[78:79]
	v_pk_add_f32 v[60:61], v[60:61], v[64:65]
	global_store_dwordx4 v[68:69], v[60:63], off
	s_nop 0
	v_lshl_add_u64 v[70:71], v[76:77], 1, s[12:13]
	v_pk_mul_f32 v[62:63], v[134:135], v[62:63]
	v_pk_mul_f32 v[60:61], v[132:133], v[60:61]
	s_waitcnt vmcnt(14)
	v_mov_b32_e32 v64, v190
	v_mov_b32_e32 v65, v191
	v_mov_b32_e32 v66, v192
	v_mov_b32_e32 v67, v193
	v_pk_add_f32 v[58:59], v[58:59], v[66:67]
	v_pk_add_f32 v[56:57], v[56:57], v[64:65]
	global_store_dwordx4 v[68:69], v[56:59], off offset:16
	v_cvt_pk_bf16_f32 v60, v60, v61
	v_cvt_pk_bf16_f32 v61, v62, v63
	v_pk_mul_f32 v[58:59], v[130:131], v[58:59]
	v_pk_mul_f32 v[56:57], v[128:129], v[56:57]
	v_cvt_pk_bf16_f32 v63, v58, v59
	v_cvt_pk_bf16_f32 v62, v56, v57
	global_store_dwordx4 v[70:71], v[60:63], off
	s_nop 0
	s_waitcnt vmcnt(13)
	v_mov_b32_e32 v56, v194
	v_mov_b32_e32 v57, v195
	v_mov_b32_e32 v58, v196
	v_mov_b32_e32 v59, v197
	v_pk_add_f32 v[54:55], v[54:55], v[58:59]
	v_pk_add_f32 v[52:53], v[52:53], v[56:57]
	global_store_dwordx4 v[68:69], v[52:55], off offset:512
	s_nop 0
	v_add_u32_e32 v60, 0x90, v152
	v_ashrrev_i32_e32 v61, 31, v60
	v_lshlrev_b64 v[60:61], 11, v[60:61]
	v_lshl_add_u64 v[60:61], v[60:61], 0, v[150:151]
	v_pk_mul_f32 v[54:55], v[122:123], v[54:55]
	v_pk_mul_f32 v[52:53], v[120:121], v[52:53]
	v_lshlrev_b64 v[62:63], 2, v[60:61]
	v_cvt_pk_bf16_f32 v52, v52, v53
	v_cvt_pk_bf16_f32 v53, v54, v55
	v_lshl_add_u64 v[64:65], s[36:37], 0, v[62:63]
	s_waitcnt vmcnt(12)
	v_mov_b32_e32 v56, v198
	v_mov_b32_e32 v57, v199
	v_mov_b32_e32 v58, v200
	v_mov_b32_e32 v59, v201
	v_pk_add_f32 v[46:47], v[46:47], v[58:59]
	v_pk_add_f32 v[44:45], v[44:45], v[56:57]
	global_store_dwordx4 v[68:69], v[44:47], off offset:528
	s_nop 1
	v_pk_mul_f32 v[46:47], v[118:119], v[46:47]
	v_pk_mul_f32 v[44:45], v[116:117], v[44:45]
	v_cvt_pk_bf16_f32 v55, v46, v47
	v_cvt_pk_bf16_f32 v54, v44, v45
	global_store_dwordx4 v[70:71], v[52:55], off offset:256
	s_nop 0
	s_waitcnt vmcnt(11)
	v_mov_b32_e32 v44, v202
	v_mov_b32_e32 v45, v203
	v_mov_b32_e32 v46, v204
	v_mov_b32_e32 v47, v205
	v_pk_add_f32 v[46:47], v[50:51], v[46:47]
	v_lshl_add_u64 v[52:53], s[10:11], 0, v[62:63]
	v_pk_add_f32 v[44:45], v[48:49], v[44:45]
	global_store_dwordx4 v[52:53], v[44:47], off
	s_nop 0
	v_lshl_add_u64 v[54:55], v[60:61], 1, s[12:13]
	v_pk_mul_f32 v[46:47], v[134:135], v[46:47]
	v_pk_mul_f32 v[44:45], v[132:133], v[44:45]
	s_waitcnt vmcnt(10)
	v_mov_b32_e32 v48, v206
	v_mov_b32_e32 v49, v207
	v_mov_b32_e32 v50, v208
	v_mov_b32_e32 v51, v209
	v_pk_add_f32 v[42:43], v[42:43], v[50:51]
	v_pk_add_f32 v[40:41], v[40:41], v[48:49]
	global_store_dwordx4 v[52:53], v[40:43], off offset:16
	v_cvt_pk_bf16_f32 v44, v44, v45
	v_cvt_pk_bf16_f32 v45, v46, v47
	v_pk_mul_f32 v[42:43], v[130:131], v[42:43]
	v_pk_mul_f32 v[40:41], v[128:129], v[40:41]
	v_cvt_pk_bf16_f32 v47, v42, v43
	v_cvt_pk_bf16_f32 v46, v40, v41
	global_store_dwordx4 v[54:55], v[44:47], off
	s_nop 0
	s_waitcnt vmcnt(9)
	v_mov_b32_e32 v40, v210
	v_mov_b32_e32 v41, v211
	v_mov_b32_e32 v42, v212
	v_mov_b32_e32 v43, v213
	v_pk_add_f32 v[38:39], v[38:39], v[42:43]
	v_pk_add_f32 v[36:37], v[36:37], v[40:41]
	global_store_dwordx4 v[52:53], v[36:39], off offset:512
	s_nop 0
	v_add_u32_e32 v44, 0xa0, v152
	v_ashrrev_i32_e32 v45, 31, v44
	v_lshlrev_b64 v[44:45], 11, v[44:45]
	v_lshl_add_u64 v[44:45], v[44:45], 0, v[150:151]
	v_pk_mul_f32 v[38:39], v[122:123], v[38:39]
	v_pk_mul_f32 v[36:37], v[120:121], v[36:37]
	v_lshlrev_b64 v[46:47], 2, v[44:45]
	v_cvt_pk_bf16_f32 v36, v36, v37
	v_cvt_pk_bf16_f32 v37, v38, v39
	v_lshl_add_u64 v[48:49], s[36:37], 0, v[46:47]
	s_waitcnt vmcnt(8)
; __device__ __forceinline__ unsigned pk2(float lo, float hi) { const f32x2 v = {lo, hi}; return __builtin_bit_cast(unsigned, __builtin_convertvector(v, bf16x2_t)); }
;     __device__ __forceinline__ void operator()(const f32x4 (&acc)[2][2][4][2], const pg::Unit& u, int wr, int wc, int fr, int fq) const {
;         const int colb = u.pn * 256 + wc * 32 + 8 * fq;
;         f32x4 gv[2][2];
; #pragma unroll
;         for (int bj = 0; bj < 2; ++bj)
; #pragma unroll
;             for (int n = 0; n < 2; ++n) gv[bj][n] = *(const f32x4*)(g + colb + bj * 128 + n * 4);
; #pragma unroll
;         for (int ai = 0; ai < 2; ++ai)
; #pragma unroll
;             for (int m = 0; m < 4; ++m) { const int row = u.pm * 256 + ai * 128 + wr * 64 + m * 16 + fr; const size_t off = (size_t)row * D_ + colb;
; #pragma unroll
;                 for (int bj = 0; bj < 2; ++bj) { f32x4 o[2];
; #pragma unroll
;                     for (int n = 0; n < 2; ++n) { const f32x4 r = *(const f32x4*)(R + off + bj * 128 + n * 4); o[n] = r + acc[ai][bj][m][n]; *(f32x4*)(O + off + bj * 128 + n * 4) = o[n]; }
;                     u32x4 w; w.x = pk2(o[0][0] * gv[bj][0][0], o[0][1] * gv[bj][0][1]); w.y = pk2(o[0][2] * gv[bj][0][2], o[0][3] * gv[bj][0][3]);
;                     w.z = pk2(o[1][0] * gv[bj][1][0], o[1][1] * gv[bj][1][1]); w.w = pk2(o[1][2] * gv[bj][1][2], o[1][3] * gv[bj][1][3]);
;                     *(u32x4*)(HBo + off + bj * 128) = w; } }
	v_mov_b32_e32 v40, v214
	v_mov_b32_e32 v41, v215
	v_mov_b32_e32 v42, v216
	v_mov_b32_e32 v43, v217
	v_pk_add_f32 v[30:31], v[30:31], v[42:43]
	v_pk_add_f32 v[28:29], v[28:29], v[40:41]
	global_store_dwordx4 v[52:53], v[28:31], off offset:528
	s_nop 1
	v_pk_mul_f32 v[30:31], v[118:119], v[30:31]
	v_pk_mul_f32 v[28:29], v[116:117], v[28:29]
	v_cvt_pk_bf16_f32 v39, v30, v31
	v_cvt_pk_bf16_f32 v38, v28, v29
	global_store_dwordx4 v[54:55], v[36:39], off offset:256
	s_nop 0
	s_waitcnt vmcnt(7)
	v_mov_b32_e32 v28, v218
	v_mov_b32_e32 v29, v219
	v_mov_b32_e32 v30, v220
	v_mov_b32_e32 v31, v221
	v_pk_add_f32 v[30:31], v[34:35], v[30:31]
	v_lshl_add_u64 v[36:37], s[10:11], 0, v[46:47]
	v_pk_add_f32 v[28:29], v[32:33], v[28:29]
	global_store_dwordx4 v[36:37], v[28:31], off
	s_nop 0
	v_lshl_add_u64 v[38:39], v[44:45], 1, s[12:13]
	v_pk_mul_f32 v[30:31], v[134:135], v[30:31]
	v_pk_mul_f32 v[28:29], v[132:133], v[28:29]
	s_waitcnt vmcnt(6)
	v_mov_b32_e32 v32, v222
	v_mov_b32_e32 v33, v223
	v_mov_b32_e32 v34, v224
	v_mov_b32_e32 v35, v225
	v_pk_add_f32 v[26:27], v[26:27], v[34:35]
	v_pk_add_f32 v[24:25], v[24:25], v[32:33]
	global_store_dwordx4 v[36:37], v[24:27], off offset:16
	v_cvt_pk_bf16_f32 v28, v28, v29
	v_cvt_pk_bf16_f32 v29, v30, v31
	v_pk_mul_f32 v[26:27], v[130:131], v[26:27]
	v_pk_mul_f32 v[24:25], v[128:129], v[24:25]
	v_cvt_pk_bf16_f32 v31, v26, v27
	v_cvt_pk_bf16_f32 v30, v24, v25
	global_store_dwordx4 v[38:39], v[28:31], off
	s_nop 0
	s_waitcnt vmcnt(5)
	v_mov_b32_e32 v24, v226
	v_mov_b32_e32 v25, v227
	v_mov_b32_e32 v26, v228
	v_mov_b32_e32 v27, v229
	v_pk_add_f32 v[22:23], v[22:23], v[26:27]
	v_pk_add_f32 v[20:21], v[20:21], v[24:25]
	global_store_dwordx4 v[36:37], v[20:23], off offset:512
	s_nop 0
	v_add_u32_e32 v28, 0xb0, v152
	v_ashrrev_i32_e32 v29, 31, v28
	v_lshlrev_b64 v[28:29], 11, v[28:29]
	v_lshl_add_u64 v[28:29], v[28:29], 0, v[150:151]
	v_pk_mul_f32 v[22:23], v[122:123], v[22:23]
	v_pk_mul_f32 v[20:21], v[120:121], v[20:21]
	v_lshlrev_b64 v[30:31], 2, v[28:29]
	v_cvt_pk_bf16_f32 v20, v20, v21
	v_cvt_pk_bf16_f32 v21, v22, v23
	v_lshl_add_u64 v[32:33], s[36:37], 0, v[30:31]
	s_waitcnt vmcnt(4)
	v_mov_b32_e32 v24, v230
	v_mov_b32_e32 v25, v231
	v_mov_b32_e32 v26, v232
	v_mov_b32_e32 v27, v233
	v_pk_add_f32 v[14:15], v[14:15], v[26:27]
	v_pk_add_f32 v[12:13], v[12:13], v[24:25]
	global_store_dwordx4 v[36:37], v[12:15], off offset:528
	s_nop 1
	v_pk_mul_f32 v[14:15], v[118:119], v[14:15]
	v_pk_mul_f32 v[12:13], v[116:117], v[12:13]
	v_cvt_pk_bf16_f32 v23, v14, v15
	v_cvt_pk_bf16_f32 v22, v12, v13
	global_store_dwordx4 v[38:39], v[20:23], off offset:256
	s_nop 0
	s_waitcnt vmcnt(3)
	v_mov_b32_e32 v12, v234
	v_mov_b32_e32 v13, v235
	v_mov_b32_e32 v14, v236
	v_mov_b32_e32 v15, v237
	v_pk_add_f32 v[14:15], v[18:19], v[14:15]
	v_lshl_add_u64 v[20:21], s[10:11], 0, v[30:31]
	v_pk_add_f32 v[12:13], v[16:17], v[12:13]
	global_store_dwordx4 v[20:21], v[12:15], off
	s_nop 0
	v_lshl_add_u64 v[22:23], v[28:29], 1, s[12:13]
	v_pk_mul_f32 v[14:15], v[134:135], v[14:15]
	v_pk_mul_f32 v[12:13], v[132:133], v[12:13]
	s_waitcnt vmcnt(2)
	v_mov_b32_e32 v16, v238
	v_mov_b32_e32 v17, v239
	v_mov_b32_e32 v18, v240
	v_mov_b32_e32 v19, v241
	v_pk_add_f32 v[10:11], v[10:11], v[18:19]
	v_pk_add_f32 v[8:9], v[8:9], v[16:17]
	global_store_dwordx4 v[20:21], v[8:11], off offset:16
	v_cvt_pk_bf16_f32 v12, v12, v13
	v_cvt_pk_bf16_f32 v13, v14, v15
	v_pk_mul_f32 v[10:11], v[130:131], v[10:11]
	v_pk_mul_f32 v[8:9], v[128:129], v[8:9]
	v_cvt_pk_bf16_f32 v15, v10, v11
	v_cvt_pk_bf16_f32 v14, v8, v9
	global_store_dwordx4 v[22:23], v[12:15], off
	s_nop 0
	s_waitcnt vmcnt(1)
	v_mov_b32_e32 v8, v242
	v_mov_b32_e32 v9, v243
	v_mov_b32_e32 v10, v244
	v_mov_b32_e32 v11, v245
	v_pk_add_f32 v[6:7], v[6:7], v[10:11]
	v_pk_add_f32 v[4:5], v[4:5], v[8:9]
	global_store_dwordx4 v[20:21], v[4:7], off offset:512
	s_nop 0
	s_waitcnt vmcnt(0)
	v_mov_b32_e32 v8, v246
	v_mov_b32_e32 v9, v247
	v_mov_b32_e32 v10, v248
	v_mov_b32_e32 v11, v249
	v_pk_add_f32 v[2:3], v[2:3], v[10:11]
	v_pk_add_f32 v[0:1], v[0:1], v[8:9]
	v_pk_mul_f32 v[6:7], v[122:123], v[6:7]
	v_pk_mul_f32 v[4:5], v[120:121], v[4:5]
	global_store_dwordx4 v[20:21], v[0:3], off offset:528
	v_cvt_pk_bf16_f32 v4, v4, v5
	v_cvt_pk_bf16_f32 v5, v6, v7
	v_pk_mul_f32 v[2:3], v[118:119], v[2:3]
	v_pk_mul_f32 v[0:1], v[116:117], v[0:1]
	v_cvt_pk_bf16_f32 v7, v2, v3
	v_cvt_pk_bf16_f32 v6, v0, v1
	global_store_dwordx4 v[22:23], v[4:7], off offset:256
	s_cbranch_vccnz .LBB0_643
	s_andn2_b64 vcc, exec, s[8:9]
	s_cbranch_vccnz .LBB0_642
	s_barrier
	s_branch .LBB0_642

; __device__ __forceinline__ float gelu_tanh(float x) { const float t = x * x; const float p = __builtin_fmaf(t, -0.10294324f, -2.3022082f); return x * __builtin_amdgcn_rcpf(1.0f + __builtin_amdgcn_exp2f(x * p)); }
; __device__ __forceinline__ u32x4 pack8(const float (&v)[8]) { u32x4 w; w.x = pk2(v[0], v[1]); w.y = pk2(v[2], v[3]); w.z = pk2(v[4], v[5]); w.w = pk2(v[6], v[7]); return w; }
;     __device__ __forceinline__ void operator()(const f32x4 (&acc)[2][2][4][2], const pg::Unit& u, int wr, int wc, int fr, int fq) const {
;         const int g = u.e, ch0 = (fq & 1) * 8; float dv[8];
; #pragma unroll
;         for (int q = 0; q < 8; ++q) dv[q] = dsk[g * 16 + ch0 + q];
; #pragma unroll
;         for (int ai = 0; ai < 2; ++ai)
; #pragma unroll
;             for (int m = 0; m < 4; ++m) { const int n = u.pm * 256 + ai * 128 + wr * 64 + m * 16 + fr;
; #pragma unroll
;                 for (int bj = 0; bj < 2; ++bj) { const int t = u.pn * 16 + 8 * bj + 2 * wc + (fq >> 1); const int token = n * 32 + t;
;                     float uu[8], o[8]; unpack8(*(const u32x4*)(U2 + ((size_t)g * T_ + token) * 16 + ch0), uu);
; #pragma unroll
;                     for (int q = 0; q < 8; ++q) o[q] = gelu_tanh(acc[ai][bj][m][q >> 2][q & 3] + dv[q] * uu[q]);
;                     *(u32x4*)(V + (((size_t)n * 128 + g) * 32 + t) * 16 + ch0) = pack8(o); } }
.LBB0_1779:
	s_lshl_b32 s88, s88, 8
	v_lshl_or_b32 v8, s30, 4, v150
	v_readlane_b32 s12, v254, 27
	v_add_u32_e32 v164, s88, v170
	v_ashrrev_i32_e32 v9, 31, v8
	v_readlane_b32 s13, v254, 28
	s_ashr_i32 s31, s30, 31
	v_ashrrev_i32_e32 v165, 31, v164
	v_readlane_b32 s26, v254, 41
	v_readlane_b32 s27, v254, 42
	v_lshl_add_u64 v[12:13], v[8:9], 2, s[12:13]
	s_lshl_b64 s[34:35], s[30:31], 5
	v_lshlrev_b32_e32 v177, 5, v164
	v_lshlrev_b64 v[8:9], 12, v[164:165]
	v_lshl_add_u32 v162, s33, 4, v173
	s_lshl_b64 s[26:27], s[30:31], 19
	v_lshl_add_u64 v[166:167], v[8:9], 0, s[34:35]
	v_add_u32_e32 v8, v177, v162
	v_ashrrev_i32_e32 v9, 31, v8
	s_add_u32 s30, s3, s26
	s_addc_u32 s31, s36, s27
	v_lshlrev_b64 v[8:9], 5, v[8:9]
	v_lshl_add_u64 v[8:9], s[30:31], 0, v[8:9]
	v_lshlrev_b32_e32 v136, 1, v150
	v_lshl_add_u64 v[8:9], v[8:9], 0, v[136:137]
	v_mov_b32_e32 v250, v8
	v_mov_b32_e32 v251, v9
	global_load_dwordx4 v[8:11], v[12:13], off offset:16
	s_nop 0
	global_load_dwordx4 v[12:15], v[12:13], off
	global_load_dwordx4 v[184:187], v[250:251], off
	global_load_dwordx4 v[188:191], v[250:251], off offset:256
	v_add_co_u32_e32 v248, vcc, 0x4000, v250
	s_nop 1
	v_addc_co_u32_e32 v249, vcc, 0, v251, vcc
	global_load_dwordx4 v[192:195], v[248:249], off
	global_load_dwordx4 v[196:199], v[248:249], off offset:256
	v_add_co_u32_e32 v248, vcc, 0x8000, v250
	s_nop 1
	v_addc_co_u32_e32 v249, vcc, 0, v251, vcc
	global_load_dwordx4 v[200:203], v[248:249], off
	global_load_dwordx4 v[204:207], v[248:249], off offset:256
	v_add_co_u32_e32 v248, vcc, 0xc000, v250
	s_nop 1
	v_addc_co_u32_e32 v249, vcc, 0, v251, vcc
	global_load_dwordx4 v[208:211], v[248:249], off
	global_load_dwordx4 v[212:215], v[248:249], off offset:256
	v_add_co_u32_e32 v248, vcc, 0x20000, v250
	s_nop 1
	v_addc_co_u32_e32 v249, vcc, 0, v251, vcc
	global_load_dwordx4 v[216:219], v[248:249], off
	global_load_dwordx4 v[220:223], v[248:249], off offset:256
	v_add_co_u32_e32 v248, vcc, 0x24000, v250
	s_nop 1
	v_addc_co_u32_e32 v249, vcc, 0, v251, vcc
	global_load_dwordx4 v[224:227], v[248:249], off
	global_load_dwordx4 v[228:231], v[248:249], off offset:256
	v_add_co_u32_e32 v248, vcc, 0x28000, v250
	s_nop 1
	v_addc_co_u32_e32 v249, vcc, 0, v251, vcc
	global_load_dwordx4 v[232:235], v[248:249], off
	global_load_dwordx4 v[236:239], v[248:249], off offset:256
	v_add_co_u32_e32 v248, vcc, 0x2c000, v250
	s_nop 1
	v_addc_co_u32_e32 v249, vcc, 0, v251, vcc
	global_load_dwordx4 v[240:243], v[248:249], off
	global_load_dwordx4 v[244:247], v[248:249], off offset:256
	s_nop 0
	s_nop 0
	s_andn2_b64 vcc, exec, s[28:29]
	v_readlane_b32 s14, v254, 29
	v_readlane_b32 s15, v254, 30
	v_readlane_b32 s16, v254, 31
	v_readlane_b32 s17, v254, 32
	v_readlane_b32 s18, v254, 33
	v_readlane_b32 s19, v254, 34
	v_readlane_b32 s20, v254, 35
	v_readlane_b32 s21, v254, 36
	v_readlane_b32 s22, v254, 37
	v_readlane_b32 s23, v254, 38
	v_readlane_b32 s24, v254, 39
	v_readlane_b32 s25, v254, 40
	s_waitcnt vmcnt(15)
	v_mov_b32_e32 v178, v184
	v_mov_b32_e32 v179, v185
	v_mov_b32_e32 v180, v186
	v_mov_b32_e32 v181, v187
	v_lshlrev_b32_e32 v182, 16, v178
	v_and_b32_e32 v183, 0xffff0000, v178
	v_pk_fma_f32 v[132:133], v[12:13], v[182:183], v[132:133]
	v_lshlrev_b32_e32 v178, 16, v179
	v_pk_mul_f32 v[182:183], v[132:133], v[132:133]
	v_and_b32_e32 v179, 0xffff0000, v179
	v_fmamk_f32 v163, v182, 0xbdd2d3e8, v168
	v_mul_f32_e32 v163, v132, v163
	v_exp_f32_e32 v163, v163
	v_pk_fma_f32 v[134:135], v[14:15], v[178:179], v[134:135]
	v_add_f32_e32 v163, 1.0, v163
	v_rcp_f32_e32 v182, v163
	v_fmamk_f32 v163, v183, 0xbdd2d3e8, v168
	v_mul_f32_e32 v163, v133, v163
	v_exp_f32_e32 v163, v163
	v_pk_mul_f32 v[178:179], v[134:135], v[134:135]
	v_add_f32_e32 v163, 1.0, v163
	v_rcp_f32_e32 v183, v163
	v_fmamk_f32 v163, v178, 0xbdd2d3e8, v168
	v_mul_f32_e32 v163, v134, v163
	v_exp_f32_e32 v163, v163
	v_pk_mul_f32 v[132:133], v[132:133], v[182:183]
	v_add_f32_e32 v163, 1.0, v163
	v_rcp_f32_e32 v178, v163
	v_fmamk_f32 v163, v179, 0xbdd2d3e8, v168
	v_mul_f32_e32 v163, v135, v163
	v_exp_f32_e32 v163, v163
	s_nop 0
	v_add_f32_e32 v163, 1.0, v163
	v_rcp_f32_e32 v179, v163
	s_nop 0
	v_pk_mul_f32 v[134:135], v[134:135], v[178:179]
	v_lshlrev_b32_e32 v178, 16, v180
	v_and_b32_e32 v179, 0xffff0000, v180
	v_pk_fma_f32 v[128:129], v[8:9], v[178:179], v[128:129]
	s_nop 0
	v_pk_mul_f32 v[178:179], v[128:129], v[128:129]
	s_nop 0
	v_fmamk_f32 v163, v178, 0xbdd2d3e8, v168
	v_mul_f32_e32 v163, v128, v163
	v_exp_f32_e32 v163, v163
	s_nop 0
	v_add_f32_e32 v163, 1.0, v163
	v_rcp_f32_e32 v178, v163
	v_fmamk_f32 v163, v179, 0xbdd2d3e8, v168
	v_mul_f32_e32 v163, v129, v163
	v_exp_f32_e32 v163, v163
	s_nop 0
	v_add_f32_e32 v163, 1.0, v163
	v_rcp_f32_e32 v179, v163
	v_ashrrev_i32_e32 v163, 31, v162
	v_pk_mul_f32 v[178:179], v[128:129], v[178:179]
	v_lshlrev_b32_e32 v128, 16, v181
	v_and_b32_e32 v129, 0xffff0000, v181
	v_pk_fma_f32 v[128:129], v[10:11], v[128:129], v[130:131]
	s_nop 0
	v_pk_mul_f32 v[130:131], v[128:129], v[128:129]
	s_nop 0
	v_fmamk_f32 v130, v130, 0xbdd2d3e8, v168
	v_fmamk_f32 v131, v131, 0xbdd2d3e8, v168
	v_mul_f32_e32 v130, v128, v130
	v_mul_f32_e32 v131, v129, v131
	v_exp_f32_e32 v130, v130
	v_exp_f32_e32 v131, v131
	v_add_f32_e32 v130, 1.0, v130
	v_add_f32_e32 v131, 1.0, v131
	v_rcp_f32_e32 v130, v130
	v_rcp_f32_e32 v131, v131
	s_nop 0
	v_pk_mul_f32 v[180:181], v[128:129], v[130:131]
	v_cvt_pk_bf16_f32 v128, v132, v133
	v_lshl_add_u64 v[132:133], v[166:167], 0, v[162:163]
	v_lshlrev_b64 v[132:133], 5, v[132:133]
	v_cvt_pk_bf16_f32 v129, v134, v135
	v_cvt_pk_bf16_f32 v130, v178, v179
	v_cvt_pk_bf16_f32 v131, v180, v181
	v_lshl_add_u64 v[132:133], v[152:153], 0, v[132:133]
	global_store_dwordx4 v[132:133], v[128:131], off
	s_nop 1
	v_add_u32_e32 v128, 8, v162
	v_add_u32_e32 v130, v177, v128
	v_ashrrev_i32_e32 v131, 31, v130
	v_lshlrev_b64 v[130:131], 5, v[130:131]
	v_lshl_add_u64 v[130:131], s[30:31], 0, v[130:131]
	v_lshl_add_u64 v[130:131], v[130:131], 0, v[136:137]
	s_nop 0
	s_waitcnt vmcnt(14)
; __device__ __forceinline__ float gelu_tanh(float x) { const float t = x * x; const float p = __builtin_fmaf(t, -0.10294324f, -2.3022082f); return x * __builtin_amdgcn_rcpf(1.0f + __builtin_amdgcn_exp2f(x * p)); }
; __device__ __forceinline__ u32x4 pack8(const float (&v)[8]) { u32x4 w; w.x = pk2(v[0], v[1]); w.y = pk2(v[2], v[3]); w.z = pk2(v[4], v[5]); w.w = pk2(v[6], v[7]); return w; }
;     __device__ __forceinline__ void operator()(const f32x4 (&acc)[2][2][4][2], const pg::Unit& u, int wr, int wc, int fr, int fq) const {
;     ...
;             for (int m = 0; m < 4; ++m) { const int n = u.pm * 256 + ai * 128 + wr * 64 + m * 16 + fr;
; #pragma unroll
;                 for (int bj = 0; bj < 2; ++bj) { const int t = u.pn * 16 + 8 * bj + 2 * wc + (fq >> 1); const int token = n * 32 + t;
;                     float uu[8], o[8]; unpack8(*(const u32x4*)(U2 + ((size_t)g * T_ + token) * 16 + ch0), uu);
; #pragma unroll
;                     for (int q = 0; q < 8; ++q) o[q] = gelu_tanh(acc[ai][bj][m][q >> 2][q & 3] + dv[q] * uu[q]);
;                     *(u32x4*)(V + (((size_t)n * 128 + g) * 32 + t) * 16 + ch0) = pack8(o); } }
	v_mov_b32_e32 v130, v188
	v_mov_b32_e32 v131, v189
	v_mov_b32_e32 v132, v190
	v_mov_b32_e32 v133, v191
	v_lshlrev_b32_e32 v134, 16, v130
	v_and_b32_e32 v135, 0xffff0000, v130
	v_pk_fma_f32 v[124:125], v[12:13], v[134:135], v[124:125]
	v_lshlrev_b32_e32 v130, 16, v131
	v_pk_mul_f32 v[134:135], v[124:125], v[124:125]
	v_and_b32_e32 v131, 0xffff0000, v131
	v_fmamk_f32 v129, v134, 0xbdd2d3e8, v168
	v_mul_f32_e32 v129, v124, v129
	v_exp_f32_e32 v129, v129
	v_pk_fma_f32 v[126:127], v[14:15], v[130:131], v[126:127]
	v_add_f32_e32 v129, 1.0, v129
	v_rcp_f32_e32 v134, v129
	v_fmamk_f32 v129, v135, 0xbdd2d3e8, v168
	v_mul_f32_e32 v129, v125, v129
	v_exp_f32_e32 v129, v129
	v_pk_mul_f32 v[130:131], v[126:127], v[126:127]
	v_add_f32_e32 v129, 1.0, v129
	v_rcp_f32_e32 v135, v129
	v_fmamk_f32 v129, v130, 0xbdd2d3e8, v168
	v_mul_f32_e32 v129, v126, v129
	v_exp_f32_e32 v129, v129
	v_pk_mul_f32 v[124:125], v[124:125], v[134:135]
	v_add_f32_e32 v129, 1.0, v129
	v_rcp_f32_e32 v130, v129
	v_fmamk_f32 v129, v131, 0xbdd2d3e8, v168
	v_mul_f32_e32 v129, v127, v129
	v_exp_f32_e32 v129, v129
	s_nop 0
	v_add_f32_e32 v129, 1.0, v129
	v_rcp_f32_e32 v131, v129
	s_nop 0
	v_pk_mul_f32 v[126:127], v[126:127], v[130:131]
	v_lshlrev_b32_e32 v130, 16, v132
	v_and_b32_e32 v131, 0xffff0000, v132
	v_pk_fma_f32 v[120:121], v[8:9], v[130:131], v[120:121]
	s_nop 0
	v_pk_mul_f32 v[130:131], v[120:121], v[120:121]
	s_nop 0
	v_fmamk_f32 v129, v130, 0xbdd2d3e8, v168
	v_mul_f32_e32 v129, v120, v129
	v_exp_f32_e32 v129, v129
	s_nop 0
	v_add_f32_e32 v129, 1.0, v129
	v_rcp_f32_e32 v130, v129
	v_fmamk_f32 v129, v131, 0xbdd2d3e8, v168
	v_mul_f32_e32 v129, v121, v129
	v_exp_f32_e32 v129, v129
	s_nop 0
	v_add_f32_e32 v129, 1.0, v129
	v_rcp_f32_e32 v131, v129
	v_ashrrev_i32_e32 v129, 31, v128
	v_pk_mul_f32 v[130:131], v[120:121], v[130:131]
	v_lshlrev_b32_e32 v120, 16, v133
	v_and_b32_e32 v121, 0xffff0000, v133
	v_pk_fma_f32 v[120:121], v[10:11], v[120:121], v[122:123]
	s_nop 0
	v_pk_mul_f32 v[122:123], v[120:121], v[120:121]
	s_nop 0
	v_fmamk_f32 v122, v122, 0xbdd2d3e8, v168
	v_fmamk_f32 v123, v123, 0xbdd2d3e8, v168
	v_mul_f32_e32 v122, v120, v122
	v_mul_f32_e32 v123, v121, v123
	v_exp_f32_e32 v122, v122
	v_exp_f32_e32 v123, v123
	v_add_f32_e32 v122, 1.0, v122
	v_add_f32_e32 v123, 1.0, v123
	v_rcp_f32_e32 v122, v122
	v_rcp_f32_e32 v123, v123
	s_nop 0
	v_pk_mul_f32 v[132:133], v[120:121], v[122:123]
	v_cvt_pk_bf16_f32 v120, v124, v125
	v_lshl_add_u64 v[124:125], v[166:167], 0, v[128:129]
	v_lshlrev_b64 v[124:125], 5, v[124:125]
	v_cvt_pk_bf16_f32 v121, v126, v127
	v_cvt_pk_bf16_f32 v122, v130, v131
	v_cvt_pk_bf16_f32 v123, v132, v133
	v_lshl_add_u64 v[124:125], v[152:153], 0, v[124:125]
	global_store_dwordx4 v[124:125], v[120:123], off
	s_nop 1
	v_add_u32_e32 v120, s88, v174
	v_lshlrev_b32_e32 v124, 5, v120
	v_add_u32_e32 v122, v124, v162
	v_ashrrev_i32_e32 v123, 31, v122
	v_lshlrev_b64 v[122:123], 5, v[122:123]
	v_lshl_add_u64 v[122:123], s[30:31], 0, v[122:123]
	v_lshl_add_u64 v[122:123], v[122:123], 0, v[136:137]
	v_ashrrev_i32_e32 v121, 31, v120
	v_lshlrev_b64 v[120:121], 12, v[120:121]
	v_lshl_add_u64 v[120:121], v[120:121], 0, s[34:35]
	s_nop 0
	s_waitcnt vmcnt(13)
	v_mov_b32_e32 v130, v192
	v_mov_b32_e32 v131, v193
	v_mov_b32_e32 v132, v194
	v_mov_b32_e32 v133, v195
	v_lshlrev_b32_e32 v122, 16, v130
	v_and_b32_e32 v123, 0xffff0000, v130
	v_pk_fma_f32 v[116:117], v[12:13], v[122:123], v[116:117]
	s_nop 0
	v_pk_mul_f32 v[122:123], v[116:117], v[116:117]
	s_nop 0
	v_fmamk_f32 v122, v122, 0xbdd2d3e8, v168
	v_fmamk_f32 v123, v123, 0xbdd2d3e8, v168
	v_mul_f32_e32 v122, v116, v122
	v_mul_f32_e32 v123, v117, v123
	v_exp_f32_e32 v122, v122
	v_exp_f32_e32 v123, v123
	v_add_f32_e32 v122, 1.0, v122
	v_add_f32_e32 v123, 1.0, v123
	v_rcp_f32_e32 v122, v122
	v_rcp_f32_e32 v123, v123
	s_nop 0
	v_pk_mul_f32 v[116:117], v[116:117], v[122:123]
	v_lshlrev_b32_e32 v122, 16, v131
	v_and_b32_e32 v123, 0xffff0000, v131
	v_pk_fma_f32 v[118:119], v[14:15], v[122:123], v[118:119]
	s_nop 0
	v_pk_mul_f32 v[122:123], v[118:119], v[118:119]
	s_nop 0
	v_fmamk_f32 v122, v122, 0xbdd2d3e8, v168
	v_fmamk_f32 v123, v123, 0xbdd2d3e8, v168
	v_mul_f32_e32 v122, v118, v122
	v_mul_f32_e32 v123, v119, v123
	v_exp_f32_e32 v122, v122
	v_exp_f32_e32 v123, v123
	v_add_f32_e32 v122, 1.0, v122
	v_add_f32_e32 v123, 1.0, v123
	v_rcp_f32_e32 v122, v122
	v_rcp_f32_e32 v123, v123
	s_nop 0
	v_pk_mul_f32 v[118:119], v[118:119], v[122:123]
	v_lshlrev_b32_e32 v122, 16, v132
	v_and_b32_e32 v123, 0xffff0000, v132
	v_pk_fma_f32 v[112:113], v[8:9], v[122:123], v[112:113]
	s_nop 0
	v_pk_mul_f32 v[122:123], v[112:113], v[112:113]
	s_nop 0
	v_fmamk_f32 v122, v122, 0xbdd2d3e8, v168
	v_fmamk_f32 v123, v123, 0xbdd2d3e8, v168
	v_mul_f32_e32 v122, v112, v122
	v_mul_f32_e32 v123, v113, v123
	v_exp_f32_e32 v122, v122
	v_exp_f32_e32 v123, v123
	v_add_f32_e32 v122, 1.0, v122
	v_add_f32_e32 v123, 1.0, v123
	v_rcp_f32_e32 v122, v122
	v_rcp_f32_e32 v123, v123
	s_nop 0
	v_pk_mul_f32 v[122:123], v[112:113], v[122:123]
	v_lshlrev_b32_e32 v112, 16, v133
	v_and_b32_e32 v113, 0xffff0000, v133
	v_pk_fma_f32 v[112:113], v[10:11], v[112:113], v[114:115]
	s_nop 0
	v_pk_mul_f32 v[114:115], v[112:113], v[112:113]
	s_nop 0
	v_fmamk_f32 v114, v114, 0xbdd2d3e8, v168
	v_fmamk_f32 v115, v115, 0xbdd2d3e8, v168
	v_mul_f32_e32 v114, v112, v114
	v_mul_f32_e32 v115, v113, v115
	v_exp_f32_e32 v114, v114
	v_exp_f32_e32 v115, v115
	v_add_f32_e32 v114, 1.0, v114
	v_add_f32_e32 v115, 1.0, v115
	v_rcp_f32_e32 v114, v114
	v_rcp_f32_e32 v115, v115
	s_nop 0
	v_pk_mul_f32 v[126:127], v[112:113], v[114:115]
	v_cvt_pk_bf16_f32 v112, v116, v117
	v_lshl_add_u64 v[116:117], v[120:121], 0, v[162:163]
	v_lshlrev_b64 v[116:117], 5, v[116:117]
	v_cvt_pk_bf16_f32 v113, v118, v119
	v_cvt_pk_bf16_f32 v114, v122, v123
	v_cvt_pk_bf16_f32 v115, v126, v127
	v_lshl_add_u64 v[116:117], v[152:153], 0, v[116:117]
	global_store_dwordx4 v[116:117], v[112:115], off
	s_nop 1
	v_add_u32_e32 v112, v124, v128
	v_ashrrev_i32_e32 v113, 31, v112
	v_lshlrev_b64 v[112:113], 5, v[112:113]
	v_lshl_add_u64 v[112:113], s[30:31], 0, v[112:113]
	v_lshl_add_u64 v[112:113], v[112:113], 0, v[136:137]
	s_nop 0
	s_waitcnt vmcnt(12)
; __device__ __forceinline__ float gelu_tanh(float x) { const float t = x * x; const float p = __builtin_fmaf(t, -0.10294324f, -2.3022082f); return x * __builtin_amdgcn_rcpf(1.0f + __builtin_amdgcn_exp2f(x * p)); }
; __device__ __forceinline__ u32x4 pack8(const float (&v)[8]) { u32x4 w; w.x = pk2(v[0], v[1]); w.y = pk2(v[2], v[3]); w.z = pk2(v[4], v[5]); w.w = pk2(v[6], v[7]); return w; }
;     __device__ __forceinline__ void operator()(const f32x4 (&acc)[2][2][4][2], const pg::Unit& u, int wr, int wc, int fr, int fq) const {
;     ...
;             for (int m = 0; m < 4; ++m) { const int n = u.pm * 256 + ai * 128 + wr * 64 + m * 16 + fr;
; #pragma unroll
;                 for (int bj = 0; bj < 2; ++bj) { const int t = u.pn * 16 + 8 * bj + 2 * wc + (fq >> 1); const int token = n * 32 + t;
;                     float uu[8], o[8]; unpack8(*(const u32x4*)(U2 + ((size_t)g * T_ + token) * 16 + ch0), uu);
; #pragma unroll
;                     for (int q = 0; q < 8; ++q) o[q] = gelu_tanh(acc[ai][bj][m][q >> 2][q & 3] + dv[q] * uu[q]);
;                     *(u32x4*)(V + (((size_t)n * 128 + g) * 32 + t) * 16 + ch0) = pack8(o); } }
	v_mov_b32_e32 v112, v196
	v_mov_b32_e32 v113, v197
	v_mov_b32_e32 v114, v198
	v_mov_b32_e32 v115, v199
	v_lshlrev_b32_e32 v116, 16, v112
	v_and_b32_e32 v117, 0xffff0000, v112
	v_pk_fma_f32 v[108:109], v[12:13], v[116:117], v[108:109]
	s_nop 0
	v_pk_mul_f32 v[116:117], v[108:109], v[108:109]
	s_nop 0
	v_fmamk_f32 v112, v116, 0xbdd2d3e8, v168
	v_mul_f32_e32 v112, v108, v112
	v_exp_f32_e32 v112, v112
	s_nop 0
	v_add_f32_e32 v112, 1.0, v112
	v_rcp_f32_e32 v116, v112
	v_fmamk_f32 v112, v117, 0xbdd2d3e8, v168
	v_mul_f32_e32 v112, v109, v112
	v_exp_f32_e32 v112, v112
	s_nop 0
	v_add_f32_e32 v112, 1.0, v112
	v_rcp_f32_e32 v117, v112
	v_lshlrev_b32_e32 v112, 16, v113
	v_and_b32_e32 v113, 0xffff0000, v113
	v_pk_fma_f32 v[110:111], v[14:15], v[112:113], v[110:111]
	v_pk_mul_f32 v[108:109], v[108:109], v[116:117]
	v_pk_mul_f32 v[112:113], v[110:111], v[110:111]
	s_nop 0
	v_fmamk_f32 v112, v112, 0xbdd2d3e8, v168
	v_fmamk_f32 v113, v113, 0xbdd2d3e8, v168
	v_mul_f32_e32 v112, v110, v112
	v_mul_f32_e32 v113, v111, v113
	v_exp_f32_e32 v112, v112
	v_exp_f32_e32 v113, v113
	v_add_f32_e32 v112, 1.0, v112
	v_add_f32_e32 v113, 1.0, v113
	v_rcp_f32_e32 v112, v112
	v_rcp_f32_e32 v113, v113
	s_nop 0
	v_pk_mul_f32 v[110:111], v[110:111], v[112:113]
	v_lshlrev_b32_e32 v112, 16, v114
	v_and_b32_e32 v113, 0xffff0000, v114
	v_pk_fma_f32 v[104:105], v[8:9], v[112:113], v[104:105]
	s_nop 0
	v_pk_mul_f32 v[112:113], v[104:105], v[104:105]
	s_nop 0
	v_fmamk_f32 v112, v112, 0xbdd2d3e8, v168
	v_fmamk_f32 v113, v113, 0xbdd2d3e8, v168
	v_mul_f32_e32 v112, v104, v112
	v_mul_f32_e32 v113, v105, v113
	v_exp_f32_e32 v112, v112
	v_exp_f32_e32 v113, v113
	v_add_f32_e32 v112, 1.0, v112
	v_add_f32_e32 v113, 1.0, v113
	v_rcp_f32_e32 v112, v112
	v_rcp_f32_e32 v113, v113
	s_nop 0
	v_pk_mul_f32 v[112:113], v[104:105], v[112:113]
	v_lshlrev_b32_e32 v104, 16, v115
	v_and_b32_e32 v105, 0xffff0000, v115
	v_pk_fma_f32 v[104:105], v[10:11], v[104:105], v[106:107]
	s_nop 0
	v_pk_mul_f32 v[106:107], v[104:105], v[104:105]
	s_nop 0
	v_fmamk_f32 v106, v106, 0xbdd2d3e8, v168
	v_fmamk_f32 v107, v107, 0xbdd2d3e8, v168
	v_mul_f32_e32 v106, v104, v106
	v_mul_f32_e32 v107, v105, v107
	v_exp_f32_e32 v106, v106
	v_exp_f32_e32 v107, v107
	v_add_f32_e32 v106, 1.0, v106
	v_add_f32_e32 v107, 1.0, v107
	v_rcp_f32_e32 v106, v106
	v_rcp_f32_e32 v107, v107
	s_nop 0
	v_pk_mul_f32 v[114:115], v[104:105], v[106:107]
	v_cvt_pk_bf16_f32 v104, v108, v109
	v_lshl_add_u64 v[108:109], v[120:121], 0, v[128:129]
	v_lshlrev_b64 v[108:109], 5, v[108:109]
	v_cvt_pk_bf16_f32 v105, v110, v111
	v_cvt_pk_bf16_f32 v106, v112, v113
	v_cvt_pk_bf16_f32 v107, v114, v115
	v_lshl_add_u64 v[108:109], v[152:153], 0, v[108:109]
	global_store_dwordx4 v[108:109], v[104:107], off
	s_nop 1
	v_add_u32_e32 v104, s88, v175
	v_lshlrev_b32_e32 v108, 5, v104
	v_add_u32_e32 v106, v108, v162
	v_ashrrev_i32_e32 v107, 31, v106
	v_lshlrev_b64 v[106:107], 5, v[106:107]
	v_lshl_add_u64 v[106:107], s[30:31], 0, v[106:107]
	v_lshl_add_u64 v[106:107], v[106:107], 0, v[136:137]
	v_ashrrev_i32_e32 v105, 31, v104
	v_lshlrev_b64 v[104:105], 12, v[104:105]
	v_lshl_add_u64 v[104:105], v[104:105], 0, s[34:35]
	s_nop 0
	s_waitcnt vmcnt(11)
	v_mov_b32_e32 v110, v200
	v_mov_b32_e32 v111, v201
	v_mov_b32_e32 v112, v202
	v_mov_b32_e32 v113, v203
	v_lshlrev_b32_e32 v106, 16, v110
	v_and_b32_e32 v107, 0xffff0000, v110
	v_pk_fma_f32 v[100:101], v[12:13], v[106:107], v[100:101]
	s_nop 0
	v_pk_mul_f32 v[106:107], v[100:101], v[100:101]
	s_nop 0
	v_fmamk_f32 v106, v106, 0xbdd2d3e8, v168
	v_fmamk_f32 v107, v107, 0xbdd2d3e8, v168
	v_mul_f32_e32 v106, v100, v106
	v_mul_f32_e32 v107, v101, v107
	v_exp_f32_e32 v106, v106
	v_exp_f32_e32 v107, v107
	v_add_f32_e32 v106, 1.0, v106
	v_add_f32_e32 v107, 1.0, v107
	v_rcp_f32_e32 v106, v106
	v_rcp_f32_e32 v107, v107
	s_nop 0
	v_pk_mul_f32 v[100:101], v[100:101], v[106:107]
	v_lshlrev_b32_e32 v106, 16, v111
	v_and_b32_e32 v107, 0xffff0000, v111
	v_pk_fma_f32 v[102:103], v[14:15], v[106:107], v[102:103]
	s_nop 0
	v_pk_mul_f32 v[106:107], v[102:103], v[102:103]
	s_nop 0
	v_fmamk_f32 v106, v106, 0xbdd2d3e8, v168
	v_fmamk_f32 v107, v107, 0xbdd2d3e8, v168
	v_mul_f32_e32 v106, v102, v106
	v_mul_f32_e32 v107, v103, v107
	v_exp_f32_e32 v106, v106
	v_exp_f32_e32 v107, v107
	v_add_f32_e32 v106, 1.0, v106
	v_add_f32_e32 v107, 1.0, v107
	v_rcp_f32_e32 v106, v106
	v_rcp_f32_e32 v107, v107
	s_nop 0
	v_pk_mul_f32 v[102:103], v[102:103], v[106:107]
	v_lshlrev_b32_e32 v106, 16, v112
	v_and_b32_e32 v107, 0xffff0000, v112
	v_pk_fma_f32 v[96:97], v[8:9], v[106:107], v[96:97]
	s_nop 0
	v_pk_mul_f32 v[106:107], v[96:97], v[96:97]
	s_nop 0
	v_fmamk_f32 v106, v106, 0xbdd2d3e8, v168
	v_fmamk_f32 v107, v107, 0xbdd2d3e8, v168
	v_mul_f32_e32 v106, v96, v106
	v_mul_f32_e32 v107, v97, v107
	v_exp_f32_e32 v106, v106
	v_exp_f32_e32 v107, v107
	v_add_f32_e32 v106, 1.0, v106
	v_add_f32_e32 v107, 1.0, v107
	v_rcp_f32_e32 v106, v106
	v_rcp_f32_e32 v107, v107
	s_nop 0
	v_pk_mul_f32 v[106:107], v[96:97], v[106:107]
	v_lshlrev_b32_e32 v96, 16, v113
	v_and_b32_e32 v97, 0xffff0000, v113
	v_pk_fma_f32 v[96:97], v[10:11], v[96:97], v[98:99]
	s_nop 0
	v_pk_mul_f32 v[98:99], v[96:97], v[96:97]
	s_nop 0
	v_fmamk_f32 v98, v98, 0xbdd2d3e8, v168
	v_fmamk_f32 v99, v99, 0xbdd2d3e8, v168
	v_mul_f32_e32 v98, v96, v98
	v_mul_f32_e32 v99, v97, v99
	v_exp_f32_e32 v98, v98
	v_exp_f32_e32 v99, v99
	v_add_f32_e32 v98, 1.0, v98
	v_add_f32_e32 v99, 1.0, v99
	v_rcp_f32_e32 v98, v98
	v_rcp_f32_e32 v99, v99
	s_nop 0
	v_pk_mul_f32 v[110:111], v[96:97], v[98:99]
	v_cvt_pk_bf16_f32 v96, v100, v101
	v_lshl_add_u64 v[100:101], v[104:105], 0, v[162:163]
	v_lshlrev_b64 v[100:101], 5, v[100:101]
	v_cvt_pk_bf16_f32 v97, v102, v103
	v_cvt_pk_bf16_f32 v98, v106, v107
	v_cvt_pk_bf16_f32 v99, v110, v111
	v_lshl_add_u64 v[100:101], v[152:153], 0, v[100:101]
	global_store_dwordx4 v[100:101], v[96:99], off
	s_nop 1
	v_add_u32_e32 v96, v108, v128
	v_ashrrev_i32_e32 v97, 31, v96
	v_lshlrev_b64 v[96:97], 5, v[96:97]
	v_lshl_add_u64 v[96:97], s[30:31], 0, v[96:97]
	v_lshl_add_u64 v[96:97], v[96:97], 0, v[136:137]
	s_nop 0
	s_waitcnt vmcnt(10)
; __device__ __forceinline__ float gelu_tanh(float x) { const float t = x * x; const float p = __builtin_fmaf(t, -0.10294324f, -2.3022082f); return x * __builtin_amdgcn_rcpf(1.0f + __builtin_amdgcn_exp2f(x * p)); }
; __device__ __forceinline__ u32x4 pack8(const float (&v)[8]) { u32x4 w; w.x = pk2(v[0], v[1]); w.y = pk2(v[2], v[3]); w.z = pk2(v[4], v[5]); w.w = pk2(v[6], v[7]); return w; }
;     __device__ __forceinline__ void operator()(const f32x4 (&acc)[2][2][4][2], const pg::Unit& u, int wr, int wc, int fr, int fq) const {
;     ...
;             for (int m = 0; m < 4; ++m) { const int n = u.pm * 256 + ai * 128 + wr * 64 + m * 16 + fr;
; #pragma unroll
;                 for (int bj = 0; bj < 2; ++bj) { const int t = u.pn * 16 + 8 * bj + 2 * wc + (fq >> 1); const int token = n * 32 + t;
;                     float uu[8], o[8]; unpack8(*(const u32x4*)(U2 + ((size_t)g * T_ + token) * 16 + ch0), uu);
; #pragma unroll
;                     for (int q = 0; q < 8; ++q) o[q] = gelu_tanh(acc[ai][bj][m][q >> 2][q & 3] + dv[q] * uu[q]);
;                     *(u32x4*)(V + (((size_t)n * 128 + g) * 32 + t) * 16 + ch0) = pack8(o); } }
	v_mov_b32_e32 v96, v204
	v_mov_b32_e32 v97, v205
	v_mov_b32_e32 v98, v206
	v_mov_b32_e32 v99, v207
	v_lshlrev_b32_e32 v100, 16, v96
	v_and_b32_e32 v101, 0xffff0000, v96
	v_pk_fma_f32 v[92:93], v[12:13], v[100:101], v[92:93]
	s_nop 0
	v_pk_mul_f32 v[100:101], v[92:93], v[92:93]
	s_nop 0
	v_fmamk_f32 v96, v100, 0xbdd2d3e8, v168
	v_mul_f32_e32 v96, v92, v96
	v_exp_f32_e32 v96, v96
	s_nop 0
	v_add_f32_e32 v96, 1.0, v96
	v_rcp_f32_e32 v100, v96
	v_fmamk_f32 v96, v101, 0xbdd2d3e8, v168
	v_mul_f32_e32 v96, v93, v96
	v_exp_f32_e32 v96, v96
	s_nop 0
	v_add_f32_e32 v96, 1.0, v96
	v_rcp_f32_e32 v101, v96
	v_lshlrev_b32_e32 v96, 16, v97
	v_and_b32_e32 v97, 0xffff0000, v97
	v_pk_fma_f32 v[94:95], v[14:15], v[96:97], v[94:95]
	v_pk_mul_f32 v[92:93], v[92:93], v[100:101]
	v_pk_mul_f32 v[96:97], v[94:95], v[94:95]
	s_nop 0
	v_fmamk_f32 v96, v96, 0xbdd2d3e8, v168
	v_fmamk_f32 v97, v97, 0xbdd2d3e8, v168
	v_mul_f32_e32 v96, v94, v96
	v_mul_f32_e32 v97, v95, v97
	v_exp_f32_e32 v96, v96
	v_exp_f32_e32 v97, v97
	v_add_f32_e32 v96, 1.0, v96
	v_add_f32_e32 v97, 1.0, v97
	v_rcp_f32_e32 v96, v96
	v_rcp_f32_e32 v97, v97
	s_nop 0
	v_pk_mul_f32 v[94:95], v[94:95], v[96:97]
	v_lshlrev_b32_e32 v96, 16, v98
	v_and_b32_e32 v97, 0xffff0000, v98
	v_pk_fma_f32 v[88:89], v[8:9], v[96:97], v[88:89]
	s_nop 0
	v_pk_mul_f32 v[96:97], v[88:89], v[88:89]
	s_nop 0
	v_fmamk_f32 v96, v96, 0xbdd2d3e8, v168
	v_fmamk_f32 v97, v97, 0xbdd2d3e8, v168
	v_mul_f32_e32 v96, v88, v96
	v_mul_f32_e32 v97, v89, v97
	v_exp_f32_e32 v96, v96
	v_exp_f32_e32 v97, v97
	v_add_f32_e32 v96, 1.0, v96
	v_add_f32_e32 v97, 1.0, v97
	v_rcp_f32_e32 v96, v96
	v_rcp_f32_e32 v97, v97
	s_nop 0
	v_pk_mul_f32 v[96:97], v[88:89], v[96:97]
	v_lshlrev_b32_e32 v88, 16, v99
	v_and_b32_e32 v89, 0xffff0000, v99
	v_pk_fma_f32 v[88:89], v[10:11], v[88:89], v[90:91]
	s_nop 0
	v_pk_mul_f32 v[90:91], v[88:89], v[88:89]
	s_nop 0
	v_fmamk_f32 v90, v90, 0xbdd2d3e8, v168
	v_fmamk_f32 v91, v91, 0xbdd2d3e8, v168
	v_mul_f32_e32 v90, v88, v90
	v_mul_f32_e32 v91, v89, v91
	v_exp_f32_e32 v90, v90
	v_exp_f32_e32 v91, v91
	v_add_f32_e32 v90, 1.0, v90
	v_add_f32_e32 v91, 1.0, v91
	v_rcp_f32_e32 v90, v90
	v_rcp_f32_e32 v91, v91
	s_nop 0
	v_pk_mul_f32 v[98:99], v[88:89], v[90:91]
	v_cvt_pk_bf16_f32 v88, v92, v93
	v_lshl_add_u64 v[92:93], v[104:105], 0, v[128:129]
	v_lshlrev_b64 v[92:93], 5, v[92:93]
	v_cvt_pk_bf16_f32 v89, v94, v95
	v_cvt_pk_bf16_f32 v90, v96, v97
	v_cvt_pk_bf16_f32 v91, v98, v99
	v_lshl_add_u64 v[92:93], v[152:153], 0, v[92:93]
	global_store_dwordx4 v[92:93], v[88:91], off
	s_nop 1
	v_add_u32_e32 v88, s88, v176
	v_lshlrev_b32_e32 v92, 5, v88
	v_add_u32_e32 v90, v92, v162
	v_ashrrev_i32_e32 v91, 31, v90
	v_lshlrev_b64 v[90:91], 5, v[90:91]
	v_lshl_add_u64 v[90:91], s[30:31], 0, v[90:91]
	v_lshl_add_u64 v[90:91], v[90:91], 0, v[136:137]
	v_ashrrev_i32_e32 v89, 31, v88
	v_lshlrev_b64 v[88:89], 12, v[88:89]
	v_lshl_add_u64 v[88:89], v[88:89], 0, s[34:35]
	s_nop 0
	s_waitcnt vmcnt(9)
	v_mov_b32_e32 v94, v208
	v_mov_b32_e32 v95, v209
	v_mov_b32_e32 v96, v210
	v_mov_b32_e32 v97, v211
	v_lshlrev_b32_e32 v90, 16, v94
	v_and_b32_e32 v91, 0xffff0000, v94
	v_pk_fma_f32 v[84:85], v[12:13], v[90:91], v[84:85]
	s_nop 0
	v_pk_mul_f32 v[90:91], v[84:85], v[84:85]
	s_nop 0
	v_fmamk_f32 v90, v90, 0xbdd2d3e8, v168
	v_fmamk_f32 v91, v91, 0xbdd2d3e8, v168
	v_mul_f32_e32 v90, v84, v90
	v_mul_f32_e32 v91, v85, v91
	v_exp_f32_e32 v90, v90
	v_exp_f32_e32 v91, v91
	v_add_f32_e32 v90, 1.0, v90
	v_add_f32_e32 v91, 1.0, v91
	v_rcp_f32_e32 v90, v90
	v_rcp_f32_e32 v91, v91
	s_nop 0
	v_pk_mul_f32 v[84:85], v[84:85], v[90:91]
	v_lshlrev_b32_e32 v90, 16, v95
	v_and_b32_e32 v91, 0xffff0000, v95
	v_pk_fma_f32 v[86:87], v[14:15], v[90:91], v[86:87]
	s_nop 0
	v_pk_mul_f32 v[90:91], v[86:87], v[86:87]
	s_nop 0
	v_fmamk_f32 v90, v90, 0xbdd2d3e8, v168
	v_fmamk_f32 v91, v91, 0xbdd2d3e8, v168
	v_mul_f32_e32 v90, v86, v90
	v_mul_f32_e32 v91, v87, v91
	v_exp_f32_e32 v90, v90
	v_exp_f32_e32 v91, v91
	v_add_f32_e32 v90, 1.0, v90
	v_add_f32_e32 v91, 1.0, v91
	v_rcp_f32_e32 v90, v90
	v_rcp_f32_e32 v91, v91
	s_nop 0
	v_pk_mul_f32 v[86:87], v[86:87], v[90:91]
	v_lshlrev_b32_e32 v90, 16, v96
	v_and_b32_e32 v91, 0xffff0000, v96
	v_pk_fma_f32 v[80:81], v[8:9], v[90:91], v[80:81]
	s_nop 0
	v_pk_mul_f32 v[90:91], v[80:81], v[80:81]
	s_nop 0
	v_fmamk_f32 v90, v90, 0xbdd2d3e8, v168
	v_fmamk_f32 v91, v91, 0xbdd2d3e8, v168
	v_mul_f32_e32 v90, v80, v90
	v_mul_f32_e32 v91, v81, v91
	v_exp_f32_e32 v90, v90
	v_exp_f32_e32 v91, v91
	v_add_f32_e32 v90, 1.0, v90
	v_add_f32_e32 v91, 1.0, v91
	v_rcp_f32_e32 v90, v90
	v_rcp_f32_e32 v91, v91
	s_nop 0
	v_pk_mul_f32 v[90:91], v[80:81], v[90:91]
	v_lshlrev_b32_e32 v80, 16, v97
	v_and_b32_e32 v81, 0xffff0000, v97
	v_pk_fma_f32 v[80:81], v[10:11], v[80:81], v[82:83]
	s_nop 0
	v_pk_mul_f32 v[82:83], v[80:81], v[80:81]
	s_nop 0
	v_fmamk_f32 v82, v82, 0xbdd2d3e8, v168
	v_fmamk_f32 v83, v83, 0xbdd2d3e8, v168
	v_mul_f32_e32 v82, v80, v82
	v_mul_f32_e32 v83, v81, v83
	v_exp_f32_e32 v82, v82
	v_exp_f32_e32 v83, v83
	v_add_f32_e32 v82, 1.0, v82
	v_add_f32_e32 v83, 1.0, v83
	v_rcp_f32_e32 v82, v82
	v_rcp_f32_e32 v83, v83
	s_nop 0
	v_pk_mul_f32 v[94:95], v[80:81], v[82:83]
	v_cvt_pk_bf16_f32 v80, v84, v85
	v_lshl_add_u64 v[84:85], v[88:89], 0, v[162:163]
	v_lshlrev_b64 v[84:85], 5, v[84:85]
	v_cvt_pk_bf16_f32 v81, v86, v87
	v_cvt_pk_bf16_f32 v82, v90, v91
	v_cvt_pk_bf16_f32 v83, v94, v95
	v_lshl_add_u64 v[84:85], v[152:153], 0, v[84:85]
	global_store_dwordx4 v[84:85], v[80:83], off
	s_nop 1
	v_add_u32_e32 v80, v92, v128
	v_ashrrev_i32_e32 v81, 31, v80
	v_lshlrev_b64 v[80:81], 5, v[80:81]
	v_lshl_add_u64 v[80:81], s[30:31], 0, v[80:81]
	v_lshl_add_u64 v[80:81], v[80:81], 0, v[136:137]
	s_nop 0
	s_waitcnt vmcnt(8)
; __device__ __forceinline__ float gelu_tanh(float x) { const float t = x * x; const float p = __builtin_fmaf(t, -0.10294324f, -2.3022082f); return x * __builtin_amdgcn_rcpf(1.0f + __builtin_amdgcn_exp2f(x * p)); }
; __device__ __forceinline__ u32x4 pack8(const float (&v)[8]) { u32x4 w; w.x = pk2(v[0], v[1]); w.y = pk2(v[2], v[3]); w.z = pk2(v[4], v[5]); w.w = pk2(v[6], v[7]); return w; }
;     __device__ __forceinline__ void operator()(const f32x4 (&acc)[2][2][4][2], const pg::Unit& u, int wr, int wc, int fr, int fq) const {
;     ...
;             for (int m = 0; m < 4; ++m) { const int n = u.pm * 256 + ai * 128 + wr * 64 + m * 16 + fr;
; #pragma unroll
;                 for (int bj = 0; bj < 2; ++bj) { const int t = u.pn * 16 + 8 * bj + 2 * wc + (fq >> 1); const int token = n * 32 + t;
;                     float uu[8], o[8]; unpack8(*(const u32x4*)(U2 + ((size_t)g * T_ + token) * 16 + ch0), uu);
; #pragma unroll
;                     for (int q = 0; q < 8; ++q) o[q] = gelu_tanh(acc[ai][bj][m][q >> 2][q & 3] + dv[q] * uu[q]);
;                     *(u32x4*)(V + (((size_t)n * 128 + g) * 32 + t) * 16 + ch0) = pack8(o); } }
	v_mov_b32_e32 v80, v212
	v_mov_b32_e32 v81, v213
	v_mov_b32_e32 v82, v214
	v_mov_b32_e32 v83, v215
	v_lshlrev_b32_e32 v84, 16, v80
	v_and_b32_e32 v85, 0xffff0000, v80
	v_pk_fma_f32 v[76:77], v[12:13], v[84:85], v[76:77]
	s_nop 0
	v_pk_mul_f32 v[84:85], v[76:77], v[76:77]
	s_nop 0
	v_fmamk_f32 v80, v84, 0xbdd2d3e8, v168
	v_mul_f32_e32 v80, v76, v80
	v_exp_f32_e32 v80, v80
	s_nop 0
	v_add_f32_e32 v80, 1.0, v80
	v_rcp_f32_e32 v84, v80
	v_fmamk_f32 v80, v85, 0xbdd2d3e8, v168
	v_mul_f32_e32 v80, v77, v80
	v_exp_f32_e32 v80, v80
	s_nop 0
	v_add_f32_e32 v80, 1.0, v80
	v_rcp_f32_e32 v85, v80
	v_lshlrev_b32_e32 v80, 16, v81
	v_and_b32_e32 v81, 0xffff0000, v81
	v_pk_fma_f32 v[78:79], v[14:15], v[80:81], v[78:79]
	v_pk_mul_f32 v[76:77], v[76:77], v[84:85]
	v_pk_mul_f32 v[80:81], v[78:79], v[78:79]
	s_nop 0
	v_fmamk_f32 v80, v80, 0xbdd2d3e8, v168
	v_fmamk_f32 v81, v81, 0xbdd2d3e8, v168
	v_mul_f32_e32 v80, v78, v80
	v_mul_f32_e32 v81, v79, v81
	v_exp_f32_e32 v80, v80
	v_exp_f32_e32 v81, v81
	v_add_f32_e32 v80, 1.0, v80
	v_add_f32_e32 v81, 1.0, v81
	v_rcp_f32_e32 v80, v80
	v_rcp_f32_e32 v81, v81
	s_nop 0
	v_pk_mul_f32 v[78:79], v[78:79], v[80:81]
	v_lshlrev_b32_e32 v80, 16, v82
	v_and_b32_e32 v81, 0xffff0000, v82
	v_pk_fma_f32 v[72:73], v[8:9], v[80:81], v[72:73]
	s_nop 0
	v_pk_mul_f32 v[80:81], v[72:73], v[72:73]
	s_nop 0
	v_fmamk_f32 v80, v80, 0xbdd2d3e8, v168
	v_fmamk_f32 v81, v81, 0xbdd2d3e8, v168
	v_mul_f32_e32 v80, v72, v80
	v_mul_f32_e32 v81, v73, v81
	v_exp_f32_e32 v80, v80
	v_exp_f32_e32 v81, v81
	v_add_f32_e32 v80, 1.0, v80
	v_add_f32_e32 v81, 1.0, v81
	v_rcp_f32_e32 v80, v80
	v_rcp_f32_e32 v81, v81
	s_nop 0
	v_pk_mul_f32 v[80:81], v[72:73], v[80:81]
	v_lshlrev_b32_e32 v72, 16, v83
	v_and_b32_e32 v73, 0xffff0000, v83
	v_pk_fma_f32 v[72:73], v[10:11], v[72:73], v[74:75]
	s_nop 0
	v_pk_mul_f32 v[74:75], v[72:73], v[72:73]
	s_nop 0
	v_fmamk_f32 v74, v74, 0xbdd2d3e8, v168
	v_fmamk_f32 v75, v75, 0xbdd2d3e8, v168
	v_mul_f32_e32 v74, v72, v74
	v_mul_f32_e32 v75, v73, v75
	v_exp_f32_e32 v74, v74
	v_exp_f32_e32 v75, v75
	v_add_f32_e32 v74, 1.0, v74
	v_add_f32_e32 v75, 1.0, v75
	v_rcp_f32_e32 v74, v74
	v_rcp_f32_e32 v75, v75
	s_nop 0
	v_pk_mul_f32 v[82:83], v[72:73], v[74:75]
	v_cvt_pk_bf16_f32 v72, v76, v77
	v_lshl_add_u64 v[76:77], v[88:89], 0, v[128:129]
	v_lshlrev_b64 v[76:77], 5, v[76:77]
	v_cvt_pk_bf16_f32 v73, v78, v79
	v_cvt_pk_bf16_f32 v74, v80, v81
	v_cvt_pk_bf16_f32 v75, v82, v83
	v_lshl_add_u64 v[76:77], v[152:153], 0, v[76:77]
	global_store_dwordx4 v[76:77], v[72:75], off
	s_nop 1
	v_add_u32_e32 v72, 0x80, v164
	v_lshlrev_b32_e32 v76, 5, v72
	v_add_u32_e32 v74, v76, v162
	v_ashrrev_i32_e32 v75, 31, v74
	v_lshlrev_b64 v[74:75], 5, v[74:75]
	v_lshl_add_u64 v[74:75], s[30:31], 0, v[74:75]
	v_lshl_add_u64 v[74:75], v[74:75], 0, v[136:137]
	v_ashrrev_i32_e32 v73, 31, v72
	v_lshlrev_b64 v[72:73], 12, v[72:73]
	v_lshl_add_u64 v[72:73], v[72:73], 0, s[34:35]
	s_nop 0
	s_waitcnt vmcnt(7)
	v_mov_b32_e32 v78, v216
	v_mov_b32_e32 v79, v217
	v_mov_b32_e32 v80, v218
	v_mov_b32_e32 v81, v219
	v_lshlrev_b32_e32 v74, 16, v78
	v_and_b32_e32 v75, 0xffff0000, v78
	v_pk_fma_f32 v[68:69], v[12:13], v[74:75], v[68:69]
	s_nop 0
	v_pk_mul_f32 v[74:75], v[68:69], v[68:69]
	s_nop 0
	v_fmamk_f32 v74, v74, 0xbdd2d3e8, v168
	v_fmamk_f32 v75, v75, 0xbdd2d3e8, v168
	v_mul_f32_e32 v74, v68, v74
	v_mul_f32_e32 v75, v69, v75
	v_exp_f32_e32 v74, v74
	v_exp_f32_e32 v75, v75
	v_add_f32_e32 v74, 1.0, v74
	v_add_f32_e32 v75, 1.0, v75
	v_rcp_f32_e32 v74, v74
	v_rcp_f32_e32 v75, v75
	s_nop 0
	v_pk_mul_f32 v[68:69], v[68:69], v[74:75]
	v_lshlrev_b32_e32 v74, 16, v79
	v_and_b32_e32 v75, 0xffff0000, v79
	v_pk_fma_f32 v[70:71], v[14:15], v[74:75], v[70:71]
	s_nop 0
	v_pk_mul_f32 v[74:75], v[70:71], v[70:71]
	s_nop 0
	v_fmamk_f32 v74, v74, 0xbdd2d3e8, v168
	v_fmamk_f32 v75, v75, 0xbdd2d3e8, v168
	v_mul_f32_e32 v74, v70, v74
	v_mul_f32_e32 v75, v71, v75
	v_exp_f32_e32 v74, v74
	v_exp_f32_e32 v75, v75
	v_add_f32_e32 v74, 1.0, v74
	v_add_f32_e32 v75, 1.0, v75
	v_rcp_f32_e32 v74, v74
	v_rcp_f32_e32 v75, v75
	s_nop 0
	v_pk_mul_f32 v[70:71], v[70:71], v[74:75]
	v_lshlrev_b32_e32 v74, 16, v80
	v_and_b32_e32 v75, 0xffff0000, v80
	v_pk_fma_f32 v[64:65], v[8:9], v[74:75], v[64:65]
	s_nop 0
	v_pk_mul_f32 v[74:75], v[64:65], v[64:65]
	s_nop 0
	v_fmamk_f32 v74, v74, 0xbdd2d3e8, v168
	v_fmamk_f32 v75, v75, 0xbdd2d3e8, v168
	v_mul_f32_e32 v74, v64, v74
	v_mul_f32_e32 v75, v65, v75
	v_exp_f32_e32 v74, v74
	v_exp_f32_e32 v75, v75
	v_add_f32_e32 v74, 1.0, v74
	v_add_f32_e32 v75, 1.0, v75
	v_rcp_f32_e32 v74, v74
	v_rcp_f32_e32 v75, v75
	s_nop 0
	v_pk_mul_f32 v[74:75], v[64:65], v[74:75]
	v_lshlrev_b32_e32 v64, 16, v81
	v_and_b32_e32 v65, 0xffff0000, v81
	v_pk_fma_f32 v[64:65], v[10:11], v[64:65], v[66:67]
	s_nop 0
	v_pk_mul_f32 v[66:67], v[64:65], v[64:65]
	s_nop 0
	v_fmamk_f32 v66, v66, 0xbdd2d3e8, v168
	v_fmamk_f32 v67, v67, 0xbdd2d3e8, v168
	v_mul_f32_e32 v66, v64, v66
	v_mul_f32_e32 v67, v65, v67
	v_exp_f32_e32 v66, v66
	v_exp_f32_e32 v67, v67
	v_add_f32_e32 v66, 1.0, v66
	v_add_f32_e32 v67, 1.0, v67
	v_rcp_f32_e32 v66, v66
	v_rcp_f32_e32 v67, v67
	s_nop 0
	v_pk_mul_f32 v[78:79], v[64:65], v[66:67]
	v_cvt_pk_bf16_f32 v64, v68, v69
	v_lshl_add_u64 v[68:69], v[72:73], 0, v[162:163]
	v_lshlrev_b64 v[68:69], 5, v[68:69]
	v_cvt_pk_bf16_f32 v65, v70, v71
	v_cvt_pk_bf16_f32 v66, v74, v75
	v_cvt_pk_bf16_f32 v67, v78, v79
	v_lshl_add_u64 v[68:69], v[152:153], 0, v[68:69]
	global_store_dwordx4 v[68:69], v[64:67], off
	s_nop 1
	v_add_u32_e32 v64, v76, v128
	v_ashrrev_i32_e32 v65, 31, v64
	v_lshlrev_b64 v[64:65], 5, v[64:65]
	v_lshl_add_u64 v[64:65], s[30:31], 0, v[64:65]
	v_lshl_add_u64 v[64:65], v[64:65], 0, v[136:137]
	s_nop 0
	s_waitcnt vmcnt(6)
; __device__ __forceinline__ float gelu_tanh(float x) { const float t = x * x; const float p = __builtin_fmaf(t, -0.10294324f, -2.3022082f); return x * __builtin_amdgcn_rcpf(1.0f + __builtin_amdgcn_exp2f(x * p)); }
; __device__ __forceinline__ u32x4 pack8(const float (&v)[8]) { u32x4 w; w.x = pk2(v[0], v[1]); w.y = pk2(v[2], v[3]); w.z = pk2(v[4], v[5]); w.w = pk2(v[6], v[7]); return w; }
;     __device__ __forceinline__ void operator()(const f32x4 (&acc)[2][2][4][2], const pg::Unit& u, int wr, int wc, int fr, int fq) const {
;     ...
;             for (int m = 0; m < 4; ++m) { const int n = u.pm * 256 + ai * 128 + wr * 64 + m * 16 + fr;
; #pragma unroll
;                 for (int bj = 0; bj < 2; ++bj) { const int t = u.pn * 16 + 8 * bj + 2 * wc + (fq >> 1); const int token = n * 32 + t;
;                     float uu[8], o[8]; unpack8(*(const u32x4*)(U2 + ((size_t)g * T_ + token) * 16 + ch0), uu);
; #pragma unroll
;                     for (int q = 0; q < 8; ++q) o[q] = gelu_tanh(acc[ai][bj][m][q >> 2][q & 3] + dv[q] * uu[q]);
;                     *(u32x4*)(V + (((size_t)n * 128 + g) * 32 + t) * 16 + ch0) = pack8(o); } }
	v_mov_b32_e32 v64, v220
	v_mov_b32_e32 v65, v221
	v_mov_b32_e32 v66, v222
	v_mov_b32_e32 v67, v223
	v_lshlrev_b32_e32 v68, 16, v64
	v_and_b32_e32 v69, 0xffff0000, v64
	v_pk_fma_f32 v[60:61], v[12:13], v[68:69], v[60:61]
	s_nop 0
	v_pk_mul_f32 v[68:69], v[60:61], v[60:61]
	s_nop 0
	v_fmamk_f32 v64, v68, 0xbdd2d3e8, v168
	v_mul_f32_e32 v64, v60, v64
	v_exp_f32_e32 v64, v64
	s_nop 0
	v_add_f32_e32 v64, 1.0, v64
	v_rcp_f32_e32 v68, v64
	v_fmamk_f32 v64, v69, 0xbdd2d3e8, v168
	v_mul_f32_e32 v64, v61, v64
	v_exp_f32_e32 v64, v64
	s_nop 0
	v_add_f32_e32 v64, 1.0, v64
	v_rcp_f32_e32 v69, v64
	v_lshlrev_b32_e32 v64, 16, v65
	v_and_b32_e32 v65, 0xffff0000, v65
	v_pk_fma_f32 v[62:63], v[14:15], v[64:65], v[62:63]
	v_pk_mul_f32 v[60:61], v[60:61], v[68:69]
	v_pk_mul_f32 v[64:65], v[62:63], v[62:63]
	s_nop 0
	v_fmamk_f32 v64, v64, 0xbdd2d3e8, v168
	v_fmamk_f32 v65, v65, 0xbdd2d3e8, v168
	v_mul_f32_e32 v64, v62, v64
	v_mul_f32_e32 v65, v63, v65
	v_exp_f32_e32 v64, v64
	v_exp_f32_e32 v65, v65
	v_add_f32_e32 v64, 1.0, v64
	v_add_f32_e32 v65, 1.0, v65
	v_rcp_f32_e32 v64, v64
	v_rcp_f32_e32 v65, v65
	s_nop 0
	v_pk_mul_f32 v[62:63], v[62:63], v[64:65]
	v_lshlrev_b32_e32 v64, 16, v66
	v_and_b32_e32 v65, 0xffff0000, v66
	v_pk_fma_f32 v[56:57], v[8:9], v[64:65], v[56:57]
	s_nop 0
	v_pk_mul_f32 v[64:65], v[56:57], v[56:57]
	s_nop 0
	v_fmamk_f32 v64, v64, 0xbdd2d3e8, v168
	v_fmamk_f32 v65, v65, 0xbdd2d3e8, v168
	v_mul_f32_e32 v64, v56, v64
	v_mul_f32_e32 v65, v57, v65
	v_exp_f32_e32 v64, v64
	v_exp_f32_e32 v65, v65
	v_add_f32_e32 v64, 1.0, v64
	v_add_f32_e32 v65, 1.0, v65
	v_rcp_f32_e32 v64, v64
	v_rcp_f32_e32 v65, v65
	s_nop 0
	v_pk_mul_f32 v[64:65], v[56:57], v[64:65]
	v_lshlrev_b32_e32 v56, 16, v67
	v_and_b32_e32 v57, 0xffff0000, v67
	v_pk_fma_f32 v[56:57], v[10:11], v[56:57], v[58:59]
	s_nop 0
	v_pk_mul_f32 v[58:59], v[56:57], v[56:57]
	s_nop 0
	v_fmamk_f32 v58, v58, 0xbdd2d3e8, v168
	v_fmamk_f32 v59, v59, 0xbdd2d3e8, v168
	v_mul_f32_e32 v58, v56, v58
	v_mul_f32_e32 v59, v57, v59
	v_exp_f32_e32 v58, v58
	v_exp_f32_e32 v59, v59
	v_add_f32_e32 v58, 1.0, v58
	v_add_f32_e32 v59, 1.0, v59
	v_rcp_f32_e32 v58, v58
	v_rcp_f32_e32 v59, v59
	s_nop 0
	v_pk_mul_f32 v[66:67], v[56:57], v[58:59]
	v_cvt_pk_bf16_f32 v56, v60, v61
	v_lshl_add_u64 v[60:61], v[72:73], 0, v[128:129]
	v_lshlrev_b64 v[60:61], 5, v[60:61]
	v_cvt_pk_bf16_f32 v57, v62, v63
	v_cvt_pk_bf16_f32 v58, v64, v65
	v_cvt_pk_bf16_f32 v59, v66, v67
	v_lshl_add_u64 v[60:61], v[152:153], 0, v[60:61]
	global_store_dwordx4 v[60:61], v[56:59], off
	s_nop 1
	v_add_u32_e32 v56, 0x90, v164
	v_lshlrev_b32_e32 v60, 5, v56
	v_add_u32_e32 v58, v60, v162
	v_ashrrev_i32_e32 v59, 31, v58
	v_lshlrev_b64 v[58:59], 5, v[58:59]
	v_lshl_add_u64 v[58:59], s[30:31], 0, v[58:59]
	v_lshl_add_u64 v[58:59], v[58:59], 0, v[136:137]
	v_ashrrev_i32_e32 v57, 31, v56
	v_lshlrev_b64 v[56:57], 12, v[56:57]
	v_lshl_add_u64 v[56:57], v[56:57], 0, s[34:35]
	s_nop 0
	s_waitcnt vmcnt(5)
	v_mov_b32_e32 v62, v224
	v_mov_b32_e32 v63, v225
	v_mov_b32_e32 v64, v226
	v_mov_b32_e32 v65, v227
	v_lshlrev_b32_e32 v58, 16, v62
	v_and_b32_e32 v59, 0xffff0000, v62
	v_pk_fma_f32 v[52:53], v[12:13], v[58:59], v[52:53]
	s_nop 0
	v_pk_mul_f32 v[58:59], v[52:53], v[52:53]
	s_nop 0
	v_fmamk_f32 v58, v58, 0xbdd2d3e8, v168
	v_fmamk_f32 v59, v59, 0xbdd2d3e8, v168
	v_mul_f32_e32 v58, v52, v58
	v_mul_f32_e32 v59, v53, v59
	v_exp_f32_e32 v58, v58
	v_exp_f32_e32 v59, v59
	v_add_f32_e32 v58, 1.0, v58
	v_add_f32_e32 v59, 1.0, v59
	v_rcp_f32_e32 v58, v58
	v_rcp_f32_e32 v59, v59
	s_nop 0
	v_pk_mul_f32 v[52:53], v[52:53], v[58:59]
	v_lshlrev_b32_e32 v58, 16, v63
	v_and_b32_e32 v59, 0xffff0000, v63
	v_pk_fma_f32 v[54:55], v[14:15], v[58:59], v[54:55]
	s_nop 0
	v_pk_mul_f32 v[58:59], v[54:55], v[54:55]
	s_nop 0
	v_fmamk_f32 v58, v58, 0xbdd2d3e8, v168
	v_fmamk_f32 v59, v59, 0xbdd2d3e8, v168
	v_mul_f32_e32 v58, v54, v58
	v_mul_f32_e32 v59, v55, v59
	v_exp_f32_e32 v58, v58
	v_exp_f32_e32 v59, v59
	v_add_f32_e32 v58, 1.0, v58
	v_add_f32_e32 v59, 1.0, v59
	v_rcp_f32_e32 v58, v58
	v_rcp_f32_e32 v59, v59
	s_nop 0
	v_pk_mul_f32 v[54:55], v[54:55], v[58:59]
	v_lshlrev_b32_e32 v58, 16, v64
	v_and_b32_e32 v59, 0xffff0000, v64
	v_pk_fma_f32 v[48:49], v[8:9], v[58:59], v[48:49]
	s_nop 0
	v_pk_mul_f32 v[58:59], v[48:49], v[48:49]
	s_nop 0
	v_fmamk_f32 v58, v58, 0xbdd2d3e8, v168
	v_fmamk_f32 v59, v59, 0xbdd2d3e8, v168
	v_mul_f32_e32 v58, v48, v58
	v_mul_f32_e32 v59, v49, v59
	v_exp_f32_e32 v58, v58
	v_exp_f32_e32 v59, v59
	v_add_f32_e32 v58, 1.0, v58
	v_add_f32_e32 v59, 1.0, v59
	v_rcp_f32_e32 v58, v58
	v_rcp_f32_e32 v59, v59
	s_nop 0
	v_pk_mul_f32 v[58:59], v[48:49], v[58:59]
	v_lshlrev_b32_e32 v48, 16, v65
	v_and_b32_e32 v49, 0xffff0000, v65
	v_pk_fma_f32 v[48:49], v[10:11], v[48:49], v[50:51]
	s_nop 0
	v_pk_mul_f32 v[50:51], v[48:49], v[48:49]
	s_nop 0
	v_fmamk_f32 v50, v50, 0xbdd2d3e8, v168
	v_fmamk_f32 v51, v51, 0xbdd2d3e8, v168
	v_mul_f32_e32 v50, v48, v50
	v_mul_f32_e32 v51, v49, v51
	v_exp_f32_e32 v50, v50
	v_exp_f32_e32 v51, v51
	v_add_f32_e32 v50, 1.0, v50
	v_add_f32_e32 v51, 1.0, v51
	v_rcp_f32_e32 v50, v50
	v_rcp_f32_e32 v51, v51
	s_nop 0
	v_pk_mul_f32 v[62:63], v[48:49], v[50:51]
	v_cvt_pk_bf16_f32 v48, v52, v53
	v_lshl_add_u64 v[52:53], v[56:57], 0, v[162:163]
	v_lshlrev_b64 v[52:53], 5, v[52:53]
	v_cvt_pk_bf16_f32 v49, v54, v55
	v_cvt_pk_bf16_f32 v50, v58, v59
	v_cvt_pk_bf16_f32 v51, v62, v63
	v_lshl_add_u64 v[52:53], v[152:153], 0, v[52:53]
	global_store_dwordx4 v[52:53], v[48:51], off
	s_nop 1
	v_add_u32_e32 v48, v60, v128
	v_ashrrev_i32_e32 v49, 31, v48
	v_lshlrev_b64 v[48:49], 5, v[48:49]
	v_lshl_add_u64 v[48:49], s[30:31], 0, v[48:49]
	v_lshl_add_u64 v[48:49], v[48:49], 0, v[136:137]
	s_nop 0
	s_waitcnt vmcnt(4)
; __device__ __forceinline__ float gelu_tanh(float x) { const float t = x * x; const float p = __builtin_fmaf(t, -0.10294324f, -2.3022082f); return x * __builtin_amdgcn_rcpf(1.0f + __builtin_amdgcn_exp2f(x * p)); }
; __device__ __forceinline__ u32x4 pack8(const float (&v)[8]) { u32x4 w; w.x = pk2(v[0], v[1]); w.y = pk2(v[2], v[3]); w.z = pk2(v[4], v[5]); w.w = pk2(v[6], v[7]); return w; }
;     __device__ __forceinline__ void operator()(const f32x4 (&acc)[2][2][4][2], const pg::Unit& u, int wr, int wc, int fr, int fq) const {
;     ...
;             for (int m = 0; m < 4; ++m) { const int n = u.pm * 256 + ai * 128 + wr * 64 + m * 16 + fr;
; #pragma unroll
;                 for (int bj = 0; bj < 2; ++bj) { const int t = u.pn * 16 + 8 * bj + 2 * wc + (fq >> 1); const int token = n * 32 + t;
;                     float uu[8], o[8]; unpack8(*(const u32x4*)(U2 + ((size_t)g * T_ + token) * 16 + ch0), uu);
; #pragma unroll
;                     for (int q = 0; q < 8; ++q) o[q] = gelu_tanh(acc[ai][bj][m][q >> 2][q & 3] + dv[q] * uu[q]);
;                     *(u32x4*)(V + (((size_t)n * 128 + g) * 32 + t) * 16 + ch0) = pack8(o); } }
	v_mov_b32_e32 v48, v228
	v_mov_b32_e32 v49, v229
	v_mov_b32_e32 v50, v230
	v_mov_b32_e32 v51, v231
	v_lshlrev_b32_e32 v52, 16, v48
	v_and_b32_e32 v53, 0xffff0000, v48
	v_pk_fma_f32 v[44:45], v[12:13], v[52:53], v[44:45]
	s_nop 0
	v_pk_mul_f32 v[52:53], v[44:45], v[44:45]
	s_nop 0
	v_fmamk_f32 v48, v52, 0xbdd2d3e8, v168
	v_mul_f32_e32 v48, v44, v48
	v_exp_f32_e32 v48, v48
	s_nop 0
	v_add_f32_e32 v48, 1.0, v48
	v_rcp_f32_e32 v52, v48
	v_fmamk_f32 v48, v53, 0xbdd2d3e8, v168
	v_mul_f32_e32 v48, v45, v48
	v_exp_f32_e32 v48, v48
	s_nop 0
	v_add_f32_e32 v48, 1.0, v48
	v_rcp_f32_e32 v53, v48
	v_lshlrev_b32_e32 v48, 16, v49
	v_and_b32_e32 v49, 0xffff0000, v49
	v_pk_fma_f32 v[46:47], v[14:15], v[48:49], v[46:47]
	v_pk_mul_f32 v[44:45], v[44:45], v[52:53]
	v_pk_mul_f32 v[48:49], v[46:47], v[46:47]
	s_nop 0
	v_fmamk_f32 v48, v48, 0xbdd2d3e8, v168
	v_fmamk_f32 v49, v49, 0xbdd2d3e8, v168
	v_mul_f32_e32 v48, v46, v48
	v_mul_f32_e32 v49, v47, v49
	v_exp_f32_e32 v48, v48
	v_exp_f32_e32 v49, v49
	v_add_f32_e32 v48, 1.0, v48
	v_add_f32_e32 v49, 1.0, v49
	v_rcp_f32_e32 v48, v48
	v_rcp_f32_e32 v49, v49
	s_nop 0
	v_pk_mul_f32 v[46:47], v[46:47], v[48:49]
	v_lshlrev_b32_e32 v48, 16, v50
	v_and_b32_e32 v49, 0xffff0000, v50
	v_pk_fma_f32 v[40:41], v[8:9], v[48:49], v[40:41]
	s_nop 0
	v_pk_mul_f32 v[48:49], v[40:41], v[40:41]
	s_nop 0
	v_fmamk_f32 v48, v48, 0xbdd2d3e8, v168
	v_fmamk_f32 v49, v49, 0xbdd2d3e8, v168
	v_mul_f32_e32 v48, v40, v48
	v_mul_f32_e32 v49, v41, v49
	v_exp_f32_e32 v48, v48
	v_exp_f32_e32 v49, v49
	v_add_f32_e32 v48, 1.0, v48
	v_add_f32_e32 v49, 1.0, v49
	v_rcp_f32_e32 v48, v48
	v_rcp_f32_e32 v49, v49
	s_nop 0
	v_pk_mul_f32 v[48:49], v[40:41], v[48:49]
	v_lshlrev_b32_e32 v40, 16, v51
	v_and_b32_e32 v41, 0xffff0000, v51
	v_pk_fma_f32 v[40:41], v[10:11], v[40:41], v[42:43]
	s_nop 0
	v_pk_mul_f32 v[42:43], v[40:41], v[40:41]
	s_nop 0
	v_fmamk_f32 v42, v42, 0xbdd2d3e8, v168
	v_fmamk_f32 v43, v43, 0xbdd2d3e8, v168
	v_mul_f32_e32 v42, v40, v42
	v_mul_f32_e32 v43, v41, v43
	v_exp_f32_e32 v42, v42
	v_exp_f32_e32 v43, v43
	v_add_f32_e32 v42, 1.0, v42
	v_add_f32_e32 v43, 1.0, v43
	v_rcp_f32_e32 v42, v42
	v_rcp_f32_e32 v43, v43
	s_nop 0
	v_pk_mul_f32 v[50:51], v[40:41], v[42:43]
	v_cvt_pk_bf16_f32 v40, v44, v45
	v_lshl_add_u64 v[44:45], v[56:57], 0, v[128:129]
	v_lshlrev_b64 v[44:45], 5, v[44:45]
	v_cvt_pk_bf16_f32 v41, v46, v47
	v_cvt_pk_bf16_f32 v42, v48, v49
	v_cvt_pk_bf16_f32 v43, v50, v51
	v_lshl_add_u64 v[44:45], v[152:153], 0, v[44:45]
	global_store_dwordx4 v[44:45], v[40:43], off
	s_nop 1
	v_add_u32_e32 v40, 0xa0, v164
	v_lshlrev_b32_e32 v44, 5, v40
	v_add_u32_e32 v42, v44, v162
	v_ashrrev_i32_e32 v43, 31, v42
	v_lshlrev_b64 v[42:43], 5, v[42:43]
	v_lshl_add_u64 v[42:43], s[30:31], 0, v[42:43]
	v_lshl_add_u64 v[42:43], v[42:43], 0, v[136:137]
	v_ashrrev_i32_e32 v41, 31, v40
	v_lshlrev_b64 v[40:41], 12, v[40:41]
	v_lshl_add_u64 v[40:41], v[40:41], 0, s[34:35]
	s_nop 0
	s_waitcnt vmcnt(3)
	v_mov_b32_e32 v46, v232
	v_mov_b32_e32 v47, v233
	v_mov_b32_e32 v48, v234
	v_mov_b32_e32 v49, v235
	v_lshlrev_b32_e32 v42, 16, v46
	v_and_b32_e32 v43, 0xffff0000, v46
	v_pk_fma_f32 v[36:37], v[12:13], v[42:43], v[36:37]
	s_nop 0
	v_pk_mul_f32 v[42:43], v[36:37], v[36:37]
	s_nop 0
	v_fmamk_f32 v42, v42, 0xbdd2d3e8, v168
	v_fmamk_f32 v43, v43, 0xbdd2d3e8, v168
	v_mul_f32_e32 v42, v36, v42
	v_mul_f32_e32 v43, v37, v43
	v_exp_f32_e32 v42, v42
	v_exp_f32_e32 v43, v43
	v_add_f32_e32 v42, 1.0, v42
	v_add_f32_e32 v43, 1.0, v43
	v_rcp_f32_e32 v42, v42
	v_rcp_f32_e32 v43, v43
	s_nop 0
	v_pk_mul_f32 v[36:37], v[36:37], v[42:43]
	v_lshlrev_b32_e32 v42, 16, v47
	v_and_b32_e32 v43, 0xffff0000, v47
	v_pk_fma_f32 v[38:39], v[14:15], v[42:43], v[38:39]
	s_nop 0
	v_pk_mul_f32 v[42:43], v[38:39], v[38:39]
	s_nop 0
	v_fmamk_f32 v42, v42, 0xbdd2d3e8, v168
	v_fmamk_f32 v43, v43, 0xbdd2d3e8, v168
	v_mul_f32_e32 v42, v38, v42
	v_mul_f32_e32 v43, v39, v43
	v_exp_f32_e32 v42, v42
	v_exp_f32_e32 v43, v43
	v_add_f32_e32 v42, 1.0, v42
	v_add_f32_e32 v43, 1.0, v43
	v_rcp_f32_e32 v42, v42
	v_rcp_f32_e32 v43, v43
	s_nop 0
	v_pk_mul_f32 v[38:39], v[38:39], v[42:43]
	v_lshlrev_b32_e32 v42, 16, v48
	v_and_b32_e32 v43, 0xffff0000, v48
	v_pk_fma_f32 v[32:33], v[8:9], v[42:43], v[32:33]
	s_nop 0
	v_pk_mul_f32 v[42:43], v[32:33], v[32:33]
	s_nop 0
	v_fmamk_f32 v42, v42, 0xbdd2d3e8, v168
	v_fmamk_f32 v43, v43, 0xbdd2d3e8, v168
	v_mul_f32_e32 v42, v32, v42
	v_mul_f32_e32 v43, v33, v43
	v_exp_f32_e32 v42, v42
	v_exp_f32_e32 v43, v43
	v_add_f32_e32 v42, 1.0, v42
	v_add_f32_e32 v43, 1.0, v43
	v_rcp_f32_e32 v42, v42
	v_rcp_f32_e32 v43, v43
	s_nop 0
	v_pk_mul_f32 v[42:43], v[32:33], v[42:43]
	v_lshlrev_b32_e32 v32, 16, v49
	v_and_b32_e32 v33, 0xffff0000, v49
	v_pk_fma_f32 v[32:33], v[10:11], v[32:33], v[34:35]
	s_nop 0
	v_pk_mul_f32 v[34:35], v[32:33], v[32:33]
	s_nop 0
	v_fmamk_f32 v34, v34, 0xbdd2d3e8, v168
	v_fmamk_f32 v35, v35, 0xbdd2d3e8, v168
	v_mul_f32_e32 v34, v32, v34
	v_mul_f32_e32 v35, v33, v35
	v_exp_f32_e32 v34, v34
	v_exp_f32_e32 v35, v35
	v_add_f32_e32 v34, 1.0, v34
	v_add_f32_e32 v35, 1.0, v35
	v_rcp_f32_e32 v34, v34
	v_rcp_f32_e32 v35, v35
	s_nop 0
	v_pk_mul_f32 v[46:47], v[32:33], v[34:35]
	v_cvt_pk_bf16_f32 v32, v36, v37
	v_lshl_add_u64 v[36:37], v[40:41], 0, v[162:163]
	v_lshlrev_b64 v[36:37], 5, v[36:37]
	v_cvt_pk_bf16_f32 v33, v38, v39
	v_cvt_pk_bf16_f32 v34, v42, v43
	v_cvt_pk_bf16_f32 v35, v46, v47
	v_lshl_add_u64 v[36:37], v[152:153], 0, v[36:37]
	global_store_dwordx4 v[36:37], v[32:35], off
	s_nop 1
	v_add_u32_e32 v32, v44, v128
	v_ashrrev_i32_e32 v33, 31, v32
	v_lshlrev_b64 v[32:33], 5, v[32:33]
	v_lshl_add_u64 v[32:33], s[30:31], 0, v[32:33]
	v_lshl_add_u64 v[32:33], v[32:33], 0, v[136:137]
	s_nop 0
	s_waitcnt vmcnt(2)
; __device__ __forceinline__ float gelu_tanh(float x) { const float t = x * x; const float p = __builtin_fmaf(t, -0.10294324f, -2.3022082f); return x * __builtin_amdgcn_rcpf(1.0f + __builtin_amdgcn_exp2f(x * p)); }
; __device__ __forceinline__ u32x4 pack8(const float (&v)[8]) { u32x4 w; w.x = pk2(v[0], v[1]); w.y = pk2(v[2], v[3]); w.z = pk2(v[4], v[5]); w.w = pk2(v[6], v[7]); return w; }
;     __device__ __forceinline__ void operator()(const f32x4 (&acc)[2][2][4][2], const pg::Unit& u, int wr, int wc, int fr, int fq) const {
;     ...
;             for (int m = 0; m < 4; ++m) { const int n = u.pm * 256 + ai * 128 + wr * 64 + m * 16 + fr;
; #pragma unroll
;                 for (int bj = 0; bj < 2; ++bj) { const int t = u.pn * 16 + 8 * bj + 2 * wc + (fq >> 1); const int token = n * 32 + t;
;                     float uu[8], o[8]; unpack8(*(const u32x4*)(U2 + ((size_t)g * T_ + token) * 16 + ch0), uu);
; #pragma unroll
;                     for (int q = 0; q < 8; ++q) o[q] = gelu_tanh(acc[ai][bj][m][q >> 2][q & 3] + dv[q] * uu[q]);
;                     *(u32x4*)(V + (((size_t)n * 128 + g) * 32 + t) * 16 + ch0) = pack8(o); } }
	v_mov_b32_e32 v32, v236
	v_mov_b32_e32 v33, v237
	v_mov_b32_e32 v34, v238
	v_mov_b32_e32 v35, v239
	v_lshlrev_b32_e32 v36, 16, v32
	v_and_b32_e32 v37, 0xffff0000, v32
	v_pk_fma_f32 v[28:29], v[12:13], v[36:37], v[28:29]
	s_nop 0
	v_pk_mul_f32 v[36:37], v[28:29], v[28:29]
	s_nop 0
	v_fmamk_f32 v32, v36, 0xbdd2d3e8, v168
	v_mul_f32_e32 v32, v28, v32
	v_exp_f32_e32 v32, v32
	s_nop 0
	v_add_f32_e32 v32, 1.0, v32
	v_rcp_f32_e32 v36, v32
	v_fmamk_f32 v32, v37, 0xbdd2d3e8, v168
	v_mul_f32_e32 v32, v29, v32
	v_exp_f32_e32 v32, v32
	s_nop 0
	v_add_f32_e32 v32, 1.0, v32
	v_rcp_f32_e32 v37, v32
	v_lshlrev_b32_e32 v32, 16, v33
	v_and_b32_e32 v33, 0xffff0000, v33
	v_pk_fma_f32 v[30:31], v[14:15], v[32:33], v[30:31]
	v_pk_mul_f32 v[28:29], v[28:29], v[36:37]
	v_pk_mul_f32 v[32:33], v[30:31], v[30:31]
	s_nop 0
	v_fmamk_f32 v32, v32, 0xbdd2d3e8, v168
	v_fmamk_f32 v33, v33, 0xbdd2d3e8, v168
	v_mul_f32_e32 v32, v30, v32
	v_mul_f32_e32 v33, v31, v33
	v_exp_f32_e32 v32, v32
	v_exp_f32_e32 v33, v33
	v_add_f32_e32 v32, 1.0, v32
	v_add_f32_e32 v33, 1.0, v33
	v_rcp_f32_e32 v32, v32
	v_rcp_f32_e32 v33, v33
	s_nop 0
	v_pk_mul_f32 v[30:31], v[30:31], v[32:33]
	v_lshlrev_b32_e32 v32, 16, v34
	v_and_b32_e32 v33, 0xffff0000, v34
	v_pk_fma_f32 v[24:25], v[8:9], v[32:33], v[24:25]
	s_nop 0
	v_pk_mul_f32 v[32:33], v[24:25], v[24:25]
	s_nop 0
	v_fmamk_f32 v32, v32, 0xbdd2d3e8, v168
	v_fmamk_f32 v33, v33, 0xbdd2d3e8, v168
	v_mul_f32_e32 v32, v24, v32
	v_mul_f32_e32 v33, v25, v33
	v_exp_f32_e32 v32, v32
	v_exp_f32_e32 v33, v33
	v_add_f32_e32 v32, 1.0, v32
	v_add_f32_e32 v33, 1.0, v33
	v_rcp_f32_e32 v32, v32
	v_rcp_f32_e32 v33, v33
	s_nop 0
	v_pk_mul_f32 v[32:33], v[24:25], v[32:33]
	v_lshlrev_b32_e32 v24, 16, v35
	v_and_b32_e32 v25, 0xffff0000, v35
	v_pk_fma_f32 v[24:25], v[10:11], v[24:25], v[26:27]
	s_nop 0
	v_pk_mul_f32 v[26:27], v[24:25], v[24:25]
	s_nop 0
	v_fmamk_f32 v26, v26, 0xbdd2d3e8, v168
	v_fmamk_f32 v27, v27, 0xbdd2d3e8, v168
	v_mul_f32_e32 v26, v24, v26
	v_mul_f32_e32 v27, v25, v27
	v_exp_f32_e32 v26, v26
	v_exp_f32_e32 v27, v27
	v_add_f32_e32 v26, 1.0, v26
	v_add_f32_e32 v27, 1.0, v27
	v_rcp_f32_e32 v26, v26
	v_rcp_f32_e32 v27, v27
	s_nop 0
	v_pk_mul_f32 v[34:35], v[24:25], v[26:27]
	v_cvt_pk_bf16_f32 v24, v28, v29
	v_lshl_add_u64 v[28:29], v[40:41], 0, v[128:129]
	v_lshlrev_b64 v[28:29], 5, v[28:29]
	v_cvt_pk_bf16_f32 v25, v30, v31
	v_cvt_pk_bf16_f32 v26, v32, v33
	v_cvt_pk_bf16_f32 v27, v34, v35
	v_lshl_add_u64 v[28:29], v[152:153], 0, v[28:29]
	global_store_dwordx4 v[28:29], v[24:27], off
	s_nop 1
	v_add_u32_e32 v24, 0xb0, v164
	v_lshlrev_b32_e32 v28, 5, v24
	v_add_u32_e32 v26, v28, v162
	v_ashrrev_i32_e32 v27, 31, v26
	v_lshlrev_b64 v[26:27], 5, v[26:27]
	v_lshl_add_u64 v[26:27], s[30:31], 0, v[26:27]
	v_lshl_add_u64 v[26:27], v[26:27], 0, v[136:137]
	v_ashrrev_i32_e32 v25, 31, v24
	v_lshlrev_b64 v[24:25], 12, v[24:25]
	v_lshl_add_u64 v[24:25], v[24:25], 0, s[34:35]
	s_nop 0
	s_waitcnt vmcnt(1)
; __device__ __forceinline__ float gelu_tanh(float x) { const float t = x * x; const float p = __builtin_fmaf(t, -0.10294324f, -2.3022082f); return x * __builtin_amdgcn_rcpf(1.0f + __builtin_amdgcn_exp2f(x * p)); }
; __device__ __forceinline__ u32x4 pack8(const float (&v)[8]) { u32x4 w; w.x = pk2(v[0], v[1]); w.y = pk2(v[2], v[3]); w.z = pk2(v[4], v[5]); w.w = pk2(v[6], v[7]); return w; }
; #define PG_BAR __builtin_amdgcn_s_barrier()
; template <class Epi, class Sched, class Hook = NoHook>
; __device__ __forceinline__ void gemm_phase_w(LAS unsigned char* lds, const Sched& S, const Epi& E, int wave_id, const Hook& HK = Hook()) {
;     ...
;         cur = nxt; ++ui;
;         if constexpr (GATHER) { gcur_00 = gnxt_00; gcur_01 = gnxt_01; gcur_10 = gnxt_10; gcur_11 = gnxt_11; }
;         if (wr == 1) PG_BAR;
;     __device__ __forceinline__ void operator()(const f32x4 (&acc)[2][2][4][2], const pg::Unit& u, int wr, int wc, int fr, int fq) const {
;     ...
;             for (int m = 0; m < 4; ++m) { const int n = u.pm * 256 + ai * 128 + wr * 64 + m * 16 + fr;
; #pragma unroll
;                 for (int bj = 0; bj < 2; ++bj) { const int t = u.pn * 16 + 8 * bj + 2 * wc + (fq >> 1); const int token = n * 32 + t;
;                     float uu[8], o[8]; unpack8(*(const u32x4*)(U2 + ((size_t)g * T_ + token) * 16 + ch0), uu);
; #pragma unroll
;                     for (int q = 0; q < 8; ++q) o[q] = gelu_tanh(acc[ai][bj][m][q >> 2][q & 3] + dv[q] * uu[q]);
;                     *(u32x4*)(V + (((size_t)n * 128 + g) * 32 + t) * 16 + ch0) = pack8(o); } }
	v_mov_b32_e32 v30, v240
	v_mov_b32_e32 v31, v241
	v_mov_b32_e32 v32, v242
	v_mov_b32_e32 v33, v243
	v_lshlrev_b32_e32 v26, 16, v30
	v_and_b32_e32 v27, 0xffff0000, v30
	v_pk_fma_f32 v[20:21], v[12:13], v[26:27], v[20:21]
	s_nop 0
	v_pk_mul_f32 v[26:27], v[20:21], v[20:21]
	s_nop 0
	v_fmamk_f32 v26, v26, 0xbdd2d3e8, v168
	v_fmamk_f32 v27, v27, 0xbdd2d3e8, v168
	v_mul_f32_e32 v26, v20, v26
	v_mul_f32_e32 v27, v21, v27
	v_exp_f32_e32 v26, v26
	v_exp_f32_e32 v27, v27
	v_add_f32_e32 v26, 1.0, v26
	v_add_f32_e32 v27, 1.0, v27
	v_rcp_f32_e32 v26, v26
	v_rcp_f32_e32 v27, v27
	s_nop 0
	v_pk_mul_f32 v[20:21], v[20:21], v[26:27]
	v_lshlrev_b32_e32 v26, 16, v31
	v_and_b32_e32 v27, 0xffff0000, v31
	v_pk_fma_f32 v[22:23], v[14:15], v[26:27], v[22:23]
	s_nop 0
	v_pk_mul_f32 v[26:27], v[22:23], v[22:23]
	s_nop 0
	v_fmamk_f32 v26, v26, 0xbdd2d3e8, v168
	v_fmamk_f32 v27, v27, 0xbdd2d3e8, v168
	v_mul_f32_e32 v26, v22, v26
	v_mul_f32_e32 v27, v23, v27
	v_exp_f32_e32 v26, v26
	v_exp_f32_e32 v27, v27
	v_add_f32_e32 v26, 1.0, v26
	v_add_f32_e32 v27, 1.0, v27
	v_rcp_f32_e32 v26, v26
	v_rcp_f32_e32 v27, v27
	s_nop 0
	v_pk_mul_f32 v[22:23], v[22:23], v[26:27]
	v_lshlrev_b32_e32 v26, 16, v32
	v_and_b32_e32 v27, 0xffff0000, v32
	v_pk_fma_f32 v[16:17], v[8:9], v[26:27], v[16:17]
	s_nop 0
	v_pk_mul_f32 v[26:27], v[16:17], v[16:17]
	s_nop 0
	v_fmamk_f32 v26, v26, 0xbdd2d3e8, v168
	v_fmamk_f32 v27, v27, 0xbdd2d3e8, v168
	v_mul_f32_e32 v26, v16, v26
	v_mul_f32_e32 v27, v17, v27
	v_exp_f32_e32 v26, v26
	v_exp_f32_e32 v27, v27
	v_add_f32_e32 v26, 1.0, v26
	v_add_f32_e32 v27, 1.0, v27
	v_rcp_f32_e32 v26, v26
	v_rcp_f32_e32 v27, v27
	s_nop 0
	v_pk_mul_f32 v[26:27], v[16:17], v[26:27]
	v_lshlrev_b32_e32 v16, 16, v33
	v_and_b32_e32 v17, 0xffff0000, v33
	v_pk_fma_f32 v[16:17], v[10:11], v[16:17], v[18:19]
	s_nop 0
	v_pk_mul_f32 v[18:19], v[16:17], v[16:17]
	s_nop 0
	v_fmamk_f32 v18, v18, 0xbdd2d3e8, v168
	v_fmamk_f32 v19, v19, 0xbdd2d3e8, v168
	v_mul_f32_e32 v18, v16, v18
	v_mul_f32_e32 v19, v17, v19
	v_exp_f32_e32 v18, v18
	v_exp_f32_e32 v19, v19
	v_add_f32_e32 v18, 1.0, v18
	v_add_f32_e32 v19, 1.0, v19
	v_rcp_f32_e32 v18, v18
	v_rcp_f32_e32 v19, v19
	s_nop 0
	v_pk_mul_f32 v[30:31], v[16:17], v[18:19]
	v_cvt_pk_bf16_f32 v16, v20, v21
	v_lshl_add_u64 v[20:21], v[24:25], 0, v[162:163]
	v_lshlrev_b64 v[20:21], 5, v[20:21]
	v_cvt_pk_bf16_f32 v17, v22, v23
	v_cvt_pk_bf16_f32 v18, v26, v27
	v_cvt_pk_bf16_f32 v19, v30, v31
	v_lshl_add_u64 v[20:21], v[152:153], 0, v[20:21]
	global_store_dwordx4 v[20:21], v[16:19], off
	s_nop 1
	v_add_u32_e32 v16, v28, v128
	v_ashrrev_i32_e32 v17, 31, v16
	v_lshlrev_b64 v[16:17], 5, v[16:17]
	v_lshl_add_u64 v[16:17], s[30:31], 0, v[16:17]
	v_lshl_add_u64 v[16:17], v[16:17], 0, v[136:137]
	s_mov_b64 s[30:31], -1
	s_nop 0
	s_waitcnt vmcnt(0)
	v_mov_b32_e32 v16, v244
	v_mov_b32_e32 v17, v245
	v_mov_b32_e32 v18, v246
	v_mov_b32_e32 v19, v247
	v_lshlrev_b32_e32 v20, 16, v16
	v_and_b32_e32 v21, 0xffff0000, v16
	v_pk_fma_f32 v[4:5], v[12:13], v[20:21], v[4:5]
	s_nop 0
	v_pk_mul_f32 v[12:13], v[4:5], v[4:5]
	s_nop 0
	v_fmamk_f32 v12, v12, 0xbdd2d3e8, v168
	v_fmamk_f32 v13, v13, 0xbdd2d3e8, v168
	v_mul_f32_e32 v12, v4, v12
	v_mul_f32_e32 v13, v5, v13
	v_exp_f32_e32 v12, v12
	v_exp_f32_e32 v13, v13
	v_add_f32_e32 v12, 1.0, v12
	v_add_f32_e32 v13, 1.0, v13
	v_rcp_f32_e32 v12, v12
	v_rcp_f32_e32 v13, v13
	s_nop 0
	v_pk_mul_f32 v[4:5], v[4:5], v[12:13]
	v_lshlrev_b32_e32 v12, 16, v17
	v_and_b32_e32 v13, 0xffff0000, v17
	v_pk_fma_f32 v[6:7], v[14:15], v[12:13], v[6:7]
	s_nop 0
	v_pk_mul_f32 v[12:13], v[6:7], v[6:7]
	s_nop 0
	v_fmamk_f32 v12, v12, 0xbdd2d3e8, v168
	v_fmamk_f32 v13, v13, 0xbdd2d3e8, v168
	v_mul_f32_e32 v12, v6, v12
	v_mul_f32_e32 v13, v7, v13
	v_exp_f32_e32 v12, v12
	v_exp_f32_e32 v13, v13
	v_add_f32_e32 v12, 1.0, v12
	v_add_f32_e32 v13, 1.0, v13
	v_rcp_f32_e32 v12, v12
	v_rcp_f32_e32 v13, v13
	s_nop 0
	v_pk_mul_f32 v[6:7], v[6:7], v[12:13]
	v_lshlrev_b32_e32 v12, 16, v18
	v_and_b32_e32 v13, 0xffff0000, v18
	v_pk_fma_f32 v[0:1], v[8:9], v[12:13], v[0:1]
	s_nop 0
	v_pk_mul_f32 v[8:9], v[0:1], v[0:1]
	s_nop 0
	v_fmamk_f32 v8, v8, 0xbdd2d3e8, v168
	v_fmamk_f32 v9, v9, 0xbdd2d3e8, v168
	v_mul_f32_e32 v8, v0, v8
	v_mul_f32_e32 v9, v1, v9
	v_exp_f32_e32 v8, v8
	v_exp_f32_e32 v9, v9
	v_add_f32_e32 v8, 1.0, v8
	v_add_f32_e32 v9, 1.0, v9
	v_rcp_f32_e32 v8, v8
	v_rcp_f32_e32 v9, v9
	s_nop 0
	v_pk_mul_f32 v[8:9], v[0:1], v[8:9]
	v_lshlrev_b32_e32 v0, 16, v19
	v_and_b32_e32 v1, 0xffff0000, v19
	v_pk_fma_f32 v[0:1], v[10:11], v[0:1], v[2:3]
	s_nop 0
	v_pk_mul_f32 v[2:3], v[0:1], v[0:1]
	s_nop 0
	v_fmamk_f32 v2, v2, 0xbdd2d3e8, v168
	v_fmamk_f32 v3, v3, 0xbdd2d3e8, v168
	v_mul_f32_e32 v2, v0, v2
	v_mul_f32_e32 v3, v1, v3
	v_exp_f32_e32 v2, v2
	v_exp_f32_e32 v3, v3
	v_add_f32_e32 v2, 1.0, v2
	v_add_f32_e32 v3, 1.0, v3
	v_rcp_f32_e32 v2, v2
	v_rcp_f32_e32 v3, v3
	s_nop 0
	v_pk_mul_f32 v[10:11], v[0:1], v[2:3]
	v_cvt_pk_bf16_f32 v0, v4, v5
	v_lshl_add_u64 v[4:5], v[24:25], 0, v[128:129]
	v_lshlrev_b64 v[4:5], 5, v[4:5]
	v_cvt_pk_bf16_f32 v1, v6, v7
	v_cvt_pk_bf16_f32 v2, v8, v9
	v_cvt_pk_bf16_f32 v3, v10, v11
	v_lshl_add_u64 v[4:5], v[152:153], 0, v[4:5]
	global_store_dwordx4 v[4:5], v[0:3], off
	s_cbranch_vccnz .LBB0_1770
	s_and_b64 vcc, exec, s[0:1]
	s_cbranch_vccnz .LBB0_1769
	s_barrier
	s_branch .LBB0_1769
